# speedup vs baseline: 1.0129x; 1.0050x over previous
.Lk4_st6_8:
	s_add_u32 s52, s10, 0x800000
	s_addc_u32 s53, s11, 0
	v_lshlrev_b64 v[130:131], 2, v[94:95]
	v_readfirstlane_b32 s14, v118
	v_lshl_add_u64 v[128:129], s[52:53], 0, v[130:131]
	s_mov_b32 m0, s14
	s_nop 0
	global_load_lds_dwordx4 v[128:129], off nt
	v_lshlrev_b64 v[130:131], 2, v[96:97]
	v_readfirstlane_b32 s14, v90
	v_lshl_add_u64 v[128:129], s[52:53], 0, v[130:131]
	s_mov_b32 m0, s14
	s_nop 0
	global_load_lds_dwordx4 v[128:129], off nt
	v_mfma_f32_16x16x32_f16 a[0:3], v[70:73], v[82:85], a[0:3]
	ds_read_b128 v[14:17], v158
	v_mfma_f32_16x16x32_f16 a[4:7], v[70:73], v[86:89], a[4:7]
	ds_read_b128 v[18:21], v160
	v_mfma_f32_16x16x32_f16 a[12:15], v[66:69], v[82:85], a[12:15]
	ds_read_b128 v[42:45], v168
	v_mfma_f32_16x16x32_f16 a[16:19], v[66:69], v[86:89], a[16:19]
	ds_read_b128 v[38:41], v168 offset:1024
	v_mfma_f32_16x16x32_f16 a[28:31], v[58:61], v[82:85], a[28:31]
	ds_read_b128 v[34:37], v168 offset:2048
	v_mfma_f32_16x16x32_f16 a[60:63], v[58:61], v[86:89], a[60:63]
	ds_read_b128 v[30:33], v168 offset:3072
	v_mfma_f32_16x16x32_f16 a[8:11], v[54:57], v[82:85], a[8:11]
	ds_read_b128 v[26:29], v168 offset:4096
	v_mfma_f32_16x16x32_f16 a[20:23], v[54:57], v[86:89], a[20:23]
	ds_read_b128 v[22:25], v168 offset:5120
	v_mfma_f32_16x16x32_f16 a[24:27], v[46:49], v[82:85], a[24:27]
	ds_read_b128 v[10:13], v168 offset:6144
	v_mfma_f32_16x16x32_f16 a[36:39], v[46:49], v[86:89], a[36:39]
	ds_read_b128 v[6:9], v168 offset:7168
	v_mfma_f32_16x16x32_f16 a[44:47], v[50:53], v[82:85], a[44:47]
	ds_read_b128 v[2:5], v168 offset:8192
	v_mfma_f32_16x16x32_f16 a[64:67], v[50:53], v[86:89], a[64:67]
	v_mfma_f32_16x16x32_f16 a[32:35], v[62:65], v[82:85], a[32:35]
	v_mfma_f32_16x16x32_f16 a[40:43], v[62:65], v[86:89], a[40:43]
	v_mfma_f32_16x16x32_f16 a[48:51], v[74:77], v[82:85], a[48:51]
	v_mfma_f32_16x16x32_f16 a[52:55], v[74:77], v[86:89], a[52:55]
	v_mfma_f32_16x16x32_f16 a[56:59], v[78:81], v[82:85], a[56:59]
	v_mfma_f32_16x16x32_f16 a[68:71], v[78:81], v[86:89], a[68:71]
	s_waitcnt lgkmcnt(8)
	v_mfma_f32_16x16x32_f16 a[0:3], v[42:45], v[14:17], a[0:3]
	ds_read_b128 v[82:85], v159
	v_mfma_f32_16x16x32_f16 a[4:7], v[42:45], v[18:21], a[4:7]
	ds_read_b128 v[86:89], v161
	s_waitcnt lgkmcnt(9)
	v_mfma_f32_16x16x32_f16 a[12:15], v[38:41], v[14:17], a[12:15]
	ds_read_b128 v[70:73], v168 offset:9216
	v_mfma_f32_16x16x32_f16 a[16:19], v[38:41], v[18:21], a[16:19]
	ds_read_b128 v[66:69], v168 offset:10240
	s_waitcnt lgkmcnt(10)
	v_mfma_f32_16x16x32_f16 a[28:31], v[34:37], v[14:17], a[28:31]
	ds_read_b128 v[58:61], v168 offset:11264
	v_mfma_f32_16x16x32_f16 a[60:63], v[34:37], v[18:21], a[60:63]
	ds_read_b128 v[54:57], v168 offset:12288
	s_waitcnt lgkmcnt(11)
	v_mfma_f32_16x16x32_f16 a[8:11], v[30:33], v[14:17], a[8:11]
	ds_read_b128 v[46:49], v168 offset:13312
	v_mfma_f32_16x16x32_f16 a[20:23], v[30:33], v[18:21], a[20:23]
	ds_read_b128 v[50:53], v168 offset:14336
	s_waitcnt lgkmcnt(12)
	v_mfma_f32_16x16x32_f16 a[24:27], v[26:29], v[14:17], a[24:27]
	ds_read_b128 v[62:65], v168 offset:15360
	v_mfma_f32_16x16x32_f16 a[36:39], v[26:29], v[18:21], a[36:39]
	ds_read_b128 v[74:77], v168 offset:16384
	s_waitcnt lgkmcnt(13)
	v_mfma_f32_16x16x32_f16 a[44:47], v[22:25], v[14:17], a[44:47]
	ds_read_b128 v[78:81], v168 offset:17408
	v_mfma_f32_16x16x32_f16 a[64:67], v[22:25], v[18:21], a[64:67]
	s_waitcnt lgkmcnt(13)
	v_mfma_f32_16x16x32_f16 a[32:35], v[10:13], v[14:17], a[32:35]
	v_mfma_f32_16x16x32_f16 a[40:43], v[10:13], v[18:21], a[40:43]
	s_waitcnt lgkmcnt(12)
	v_mfma_f32_16x16x32_f16 a[48:51], v[6:9], v[14:17], a[48:51]
	v_mfma_f32_16x16x32_f16 a[52:55], v[6:9], v[18:21], a[52:55]
	s_waitcnt lgkmcnt(11)
	v_mfma_f32_16x16x32_f16 a[56:59], v[2:5], v[14:17], a[56:59]
	v_mfma_f32_16x16x32_f16 a[68:71], v[2:5], v[18:21], a[68:71]
	s_waitcnt vmcnt(2) lgkmcnt(0)
	s_barrier
	v_add_u32_e32 v128, s16, v118
	s_nop 1
	v_readfirstlane_b32 s14, v128
	s_mov_b32 m0, s14
	s_nop 0
	global_load_lds_dwordx4 v[0:1], off nt
	v_add_u32_e32 v128, s16, v90
	s_nop 1
	v_readfirstlane_b32 s14, v128
	s_mov_b32 m0, s14
	s_nop 0
	global_load_lds_dwordx4 v[106:107], off nt
	v_add_u32_e32 v128, s16, v91
	s_nop 1
	v_readfirstlane_b32 s14, v128
	s_mov_b32 m0, s14
	s_nop 0
	global_load_lds_dwordx4 v[110:111], off nt
	v_add_u32_e32 v128, s16, v119
	s_nop 1
	v_readfirstlane_b32 s14, v128
	s_mov_b32 m0, s14
	s_nop 0
	global_load_lds_dwordx4 v[114:115], off nt
	v_mfma_f32_16x16x32_f16 a[0:3], v[70:73], v[82:85], a[0:3]
	ds_read_b128 v[14:17], v160
	v_mfma_f32_16x16x32_f16 a[4:7], v[70:73], v[86:89], a[4:7]
	ds_read_b128 v[18:21], v162
	v_mfma_f32_16x16x32_f16 a[12:15], v[66:69], v[82:85], a[12:15]
	ds_read_b128 v[42:45], v164
	v_mfma_f32_16x16x32_f16 a[16:19], v[66:69], v[86:89], a[16:19]
	ds_read_b128 v[38:41], v164 offset:1024
	v_mfma_f32_16x16x32_f16 a[28:31], v[58:61], v[82:85], a[28:31]
	ds_read_b128 v[34:37], v164 offset:2048
	v_mfma_f32_16x16x32_f16 a[60:63], v[58:61], v[86:89], a[60:63]
	ds_read_b128 v[30:33], v164 offset:3072
	v_mfma_f32_16x16x32_f16 a[8:11], v[54:57], v[82:85], a[8:11]
	ds_read_b128 v[26:29], v164 offset:4096
	v_mfma_f32_16x16x32_f16 a[20:23], v[54:57], v[86:89], a[20:23]
	ds_read_b128 v[22:25], v164 offset:5120
	v_mfma_f32_16x16x32_f16 a[24:27], v[46:49], v[82:85], a[24:27]
	ds_read_b128 v[10:13], v164 offset:6144
	v_mfma_f32_16x16x32_f16 a[36:39], v[46:49], v[86:89], a[36:39]
	ds_read_b128 v[6:9], v164 offset:7168
	v_mfma_f32_16x16x32_f16 a[44:47], v[50:53], v[82:85], a[44:47]
	ds_read_b128 v[2:5], v164 offset:8192
	v_mfma_f32_16x16x32_f16 a[64:67], v[50:53], v[86:89], a[64:67]
	v_mfma_f32_16x16x32_f16 a[32:35], v[62:65], v[82:85], a[32:35]
	v_mfma_f32_16x16x32_f16 a[40:43], v[62:65], v[86:89], a[40:43]
	v_mfma_f32_16x16x32_f16 a[48:51], v[74:77], v[82:85], a[48:51]
	v_mfma_f32_16x16x32_f16 a[52:55], v[74:77], v[86:89], a[52:55]
	v_mfma_f32_16x16x32_f16 a[56:59], v[78:81], v[82:85], a[56:59]
	v_mfma_f32_16x16x32_f16 a[68:71], v[78:81], v[86:89], a[68:71]
	s_waitcnt lgkmcnt(8)
	v_mfma_f32_16x16x32_f16 a[0:3], v[42:45], v[14:17], a[0:3]
	ds_read_b128 v[82:85], v161
	v_mfma_f32_16x16x32_f16 a[4:7], v[42:45], v[18:21], a[4:7]
	ds_read_b128 v[86:89], v163
	s_waitcnt lgkmcnt(9)
	v_mfma_f32_16x16x32_f16 a[12:15], v[38:41], v[14:17], a[12:15]
	ds_read_b128 v[70:73], v164 offset:9216
	v_mfma_f32_16x16x32_f16 a[16:19], v[38:41], v[18:21], a[16:19]
	ds_read_b128 v[66:69], v164 offset:10240
	s_waitcnt lgkmcnt(10)
	v_mfma_f32_16x16x32_f16 a[28:31], v[34:37], v[14:17], a[28:31]
	ds_read_b128 v[58:61], v164 offset:11264
	v_mfma_f32_16x16x32_f16 a[60:63], v[34:37], v[18:21], a[60:63]
	ds_read_b128 v[54:57], v164 offset:12288
	s_waitcnt lgkmcnt(11)
	v_mfma_f32_16x16x32_f16 a[8:11], v[30:33], v[14:17], a[8:11]
	ds_read_b128 v[46:49], v164 offset:13312
	v_mfma_f32_16x16x32_f16 a[20:23], v[30:33], v[18:21], a[20:23]
	ds_read_b128 v[50:53], v164 offset:14336
	s_waitcnt lgkmcnt(12)
	v_mfma_f32_16x16x32_f16 a[24:27], v[26:29], v[14:17], a[24:27]
	ds_read_b128 v[62:65], v164 offset:15360
	v_mfma_f32_16x16x32_f16 a[36:39], v[26:29], v[18:21], a[36:39]
	ds_read_b128 v[74:77], v164 offset:16384
	s_waitcnt lgkmcnt(13)
	v_mfma_f32_16x16x32_f16 a[44:47], v[22:25], v[14:17], a[44:47]
	ds_read_b128 v[78:81], v164 offset:17408
	v_mfma_f32_16x16x32_f16 a[64:67], v[22:25], v[18:21], a[64:67]
	s_waitcnt lgkmcnt(13)
	v_mfma_f32_16x16x32_f16 a[32:35], v[10:13], v[14:17], a[32:35]
	v_mfma_f32_16x16x32_f16 a[40:43], v[10:13], v[18:21], a[40:43]
	s_waitcnt lgkmcnt(12)
	v_mfma_f32_16x16x32_f16 a[48:51], v[6:9], v[14:17], a[48:51]
	v_mfma_f32_16x16x32_f16 a[52:55], v[6:9], v[18:21], a[52:55]
	s_waitcnt lgkmcnt(11)
	v_mfma_f32_16x16x32_f16 a[56:59], v[2:5], v[14:17], a[56:59]
	v_mfma_f32_16x16x32_f16 a[68:71], v[2:5], v[18:21], a[68:71]
	s_waitcnt lgkmcnt(8)
	v_mfma_f32_16x16x32_f16 a[0:3], v[70:73], v[82:85], a[0:3]
	v_mfma_f32_16x16x32_f16 a[4:7], v[70:73], v[86:89], a[4:7]
	s_waitcnt lgkmcnt(9)
	v_mfma_f32_16x16x32_f16 a[12:15], v[66:69], v[82:85], a[12:15]
	v_mfma_f32_16x16x32_f16 a[16:19], v[66:69], v[86:89], a[16:19]
	s_waitcnt lgkmcnt(10)
	v_mfma_f32_16x16x32_f16 a[28:31], v[58:61], v[82:85], a[28:31]
	v_mfma_f32_16x16x32_f16 a[60:63], v[58:61], v[86:89], a[60:63]
	s_waitcnt lgkmcnt(11)
	v_mfma_f32_16x16x32_f16 a[8:11], v[54:57], v[82:85], a[8:11]
	v_mfma_f32_16x16x32_f16 a[20:23], v[54:57], v[86:89], a[20:23]
	s_waitcnt lgkmcnt(12)
	v_mfma_f32_16x16x32_f16 a[24:27], v[46:49], v[82:85], a[24:27]
	v_mfma_f32_16x16x32_f16 a[36:39], v[46:49], v[86:89], a[36:39]
	s_waitcnt lgkmcnt(13)
	v_mfma_f32_16x16x32_f16 a[44:47], v[50:53], v[82:85], a[44:47]
	v_mfma_f32_16x16x32_f16 a[64:67], v[50:53], v[86:89], a[64:67]
	s_waitcnt lgkmcnt(13)
	v_mfma_f32_16x16x32_f16 a[32:35], v[62:65], v[82:85], a[32:35]
	v_mfma_f32_16x16x32_f16 a[40:43], v[62:65], v[86:89], a[40:43]
	s_waitcnt lgkmcnt(12)
	v_mfma_f32_16x16x32_f16 a[48:51], v[74:77], v[82:85], a[48:51]
	v_mfma_f32_16x16x32_f16 a[52:55], v[74:77], v[86:89], a[52:55]
	s_waitcnt lgkmcnt(11)
	v_mfma_f32_16x16x32_f16 a[56:59], v[78:81], v[82:85], a[56:59]
	v_mfma_f32_16x16x32_f16 a[68:71], v[78:81], v[86:89], a[68:71]
	s_waitcnt lgkmcnt(0)
	s_setprio 0
.LBB3_32:
	s_barrier
	v_accvgpr_read_b32 v140, a72
	v_lshlrev_b64 v[142:143], 2, v[94:95]
	v_lshlrev_b64 v[144:145], 2, v[96:97]
	v_lshlrev_b64 v[146:147], 2, v[98:99]
	v_lshlrev_b64 v[148:149], 2, v[100:101]
	s_add_u32 s52, s10, 0x800000
	s_addc_u32 s53, s11, 0
	v_add_u32_e32 v150, 0x0, v91
	v_lshl_add_u64 v[152:153], s[52:53], 0, v[146:147]
	s_nop 0
	v_readfirstlane_b32 s44, v150
	s_mov_b32 m0, s44
	s_nop 0
	global_load_lds_dwordx4 v[152:153], off nt
	v_add_u32_e32 v150, 0x0, v119
	v_lshl_add_u64 v[152:153], s[52:53], 0, v[148:149]
	s_nop 0
	v_readfirstlane_b32 s44, v150
	s_mov_b32 m0, s44
	s_nop 0
	global_load_lds_dwordx4 v[152:153], off nt
	s_add_u32 s52, s10, 0xc00000
	s_addc_u32 s53, s11, 0
	v_add_u32_e32 v150, 0x7000, v140
	v_lshl_add_u64 v[152:153], s[52:53], 0, v[142:143]
	s_nop 0
	v_readfirstlane_b32 s44, v150
	s_mov_b32 m0, s44
	s_nop 0
	global_load_lds_dwordx4 v[152:153], off nt
	v_add_u32_e32 v150, 0x7000, v90
	v_lshl_add_u64 v[152:153], s[52:53], 0, v[144:145]
	s_nop 0
	v_readfirstlane_b32 s44, v150
	s_mov_b32 m0, s44
	s_nop 0
	global_load_lds_dwordx4 v[152:153], off nt
	v_add_u32_e32 v150, 0x7000, v91
	v_lshl_add_u64 v[152:153], s[52:53], 0, v[146:147]
	s_nop 0
	v_readfirstlane_b32 s44, v150
	s_mov_b32 m0, s44
	s_nop 0
	global_load_lds_dwordx4 v[152:153], off nt
	v_add_u32_e32 v150, 0x7000, v119
	v_lshl_add_u64 v[152:153], s[52:53], 0, v[148:149]
	s_nop 0
	v_readfirstlane_b32 s44, v150
	s_mov_b32 m0, s44
	s_nop 0
	global_load_lds_dwordx4 v[152:153], off nt
	s_add_u32 s52, s10, 0x1000000
	s_addc_u32 s53, s11, 0
	v_add_u32_e32 v150, 0xe000, v140
	v_lshl_add_u64 v[152:153], s[52:53], 0, v[142:143]
	s_nop 0
	v_readfirstlane_b32 s44, v150
	s_mov_b32 m0, s44
	s_nop 0
	global_load_lds_dwordx4 v[152:153], off nt
	v_add_u32_e32 v150, 0xe000, v90
	v_lshl_add_u64 v[152:153], s[52:53], 0, v[144:145]
	s_nop 0
	v_readfirstlane_b32 s44, v150
	s_mov_b32 m0, s44
	s_nop 0
	global_load_lds_dwordx4 v[152:153], off nt
	v_add_u32_e32 v150, 0xe000, v91
	v_lshl_add_u64 v[152:153], s[52:53], 0, v[146:147]
	s_nop 0
	v_readfirstlane_b32 s44, v150
	s_mov_b32 m0, s44
	s_nop 0
	global_load_lds_dwordx4 v[152:153], off nt
	v_add_u32_e32 v150, 0xe000, v119
	v_lshl_add_u64 v[152:153], s[52:53], 0, v[148:149]
	s_nop 0
	v_readfirstlane_b32 s44, v150
	s_mov_b32 m0, s44
	s_nop 0
	global_load_lds_dwordx4 v[152:153], off nt
	v_lshl_add_u32 v0, v120, 5, s22
	v_or_b32_e32 v1, s23, v121
	s_movk_i32 s0, 0x7f
	v_lshl_or_b32 v7, v93, 1, v0
	s_movk_i32 s1, 0x7e
	s_nop 15
	s_nop 15
	v_cmp_eq_u32_e64 s[4:5], s1, v7
	s_nop 7
	v_cmp_gt_u32_e32 vcc, s0, v1
	v_accvgpr_read_b32 v5, a14
	v_cmp_eq_u32_e64 s[0:1], 0, v1
	v_or_b32_e32 v4, v93, v7
	v_cmp_eq_u32_e64 s[2:3], 0, v4
	v_cndmask_b32_e64 v14, v5, 0, s[0:1]
	v_accvgpr_read_b32 v5, a13
	v_cndmask_b32_e64 v22, v5, 0, s[0:1]
	v_accvgpr_read_b32 v5, a12
	v_cndmask_b32_e64 v116, v5, 0, s[0:1]
	v_accvgpr_read_b32 v5, a49
	v_cndmask_b32_e32 v16, 0, v5, vcc
	v_accvgpr_read_b32 v5, a48
	v_cndmask_b32_e32 v28, 0, v5, vcc
	v_accvgpr_read_b32 v5, a30
	v_cndmask_b32_e64 v10, v5, 0, s[0:1]
	v_accvgpr_read_b32 v5, a29
	v_cndmask_b32_e64 v24, v5, 0, s[0:1]
	v_accvgpr_read_b32 v5, a28
	v_cndmask_b32_e64 v42, v5, 0, s[0:1]
	v_accvgpr_read_b32 v5, a57
	v_cndmask_b32_e32 v20, 0, v5, vcc
	v_accvgpr_read_b32 v5, a56
	v_cndmask_b32_e32 v38, 0, v5, vcc
	v_accvgpr_read_b32 v5, a6
	v_cndmask_b32_e64 v15, v5, 0, s[0:1]
	v_accvgpr_read_b32 v5, a5
	v_cndmask_b32_e64 v23, v5, 0, s[0:1]
	v_accvgpr_read_b32 v5, a4
	v_cndmask_b32_e64 v117, v5, 0, s[0:1]
	v_accvgpr_read_b32 v5, a41
	v_cndmask_b32_e32 v17, 0, v5, vcc
	v_accvgpr_read_b32 v5, a40
	v_cndmask_b32_e32 v29, 0, v5, vcc
	v_accvgpr_read_b32 v5, a17
	v_cndmask_b32_e64 v37, v5, 0, s[0:1]
	v_accvgpr_read_b32 v5, a16
	v_cndmask_b32_e64 v47, v5, 0, s[0:1]
	v_accvgpr_read_b32 v5, a52
	v_cndmask_b32_e32 v45, 0, v5, vcc
	v_accvgpr_read_b32 v5, a68
	v_cndmask_b32_e32 v12, 0, v5, vcc
	v_accvgpr_read_b32 v5, a0
	s_or_b64 s[8:9], s[2:3], s[0:1]
	v_cmp_eq_u32_e64 s[6:7], 15, v93
	v_accvgpr_read_b32 v11, a8
	v_cndmask_b32_e64 v112, v5, 0, s[8:9]
	v_accvgpr_read_b32 v4, a67
	v_mov_b32_e32 v5, 0x90
	s_and_b64 s[4:5], s[6:7], s[4:5]
	v_mov_b64_e32 v[40:41], v[16:17]
	v_cndmask_b32_e64 v16, v11, 0, s[2:3]
	v_cndmask_b32_e64 v11, 12, v5, s[6:7]
	v_cndmask_b32_e64 v61, v4, 0, s[4:5]
	v_accvgpr_read_b32 v4, a61
	s_or_b64 s[6:7], s[4:5], s[0:1]
	v_cndmask_b32_e64 v87, v4, 0, s[6:7]
	v_accvgpr_read_b32 v4, a60
	v_cndmask_b32_e64 v86, v4, 0, s[6:7]
	v_accvgpr_read_b32 v4, a65
	v_cndmask_b32_e64 v5, v4, 0, s[4:5]
	v_accvgpr_read_b32 v4, a64
	v_cndmask_b32_e64 v4, v4, 0, s[4:5]
	s_lshl_b32 s14, s18, 2
	v_mov_b64_e32 v[32:33], v[4:5]
	v_lshl_or_b32 v4, v122, 18, s14
	v_mov_b32_e32 v5, 0
	v_mov_b64_e32 v[62:63], v[14:15]
	v_lshl_add_u64 v[14:15], s[12:13], 0, v[4:5]
	v_lshlrev_b32_e32 v4, 7, v1
	v_lshl_add_u64 v[14:15], v[4:5], 2, v[14:15]
	v_lshlrev_b32_e32 v4, 2, v7
	v_mul_u32_u24_e32 v1, 24, v122
	v_lshl_add_u64 v[54:55], v[14:15], 0, v[4:5]
	v_mbcnt_lo_u32_b32 v138, -1, 0
	v_mbcnt_hi_u32_b32 v138, -1, v138
	v_and_b32_e32 v138, 1, v138
	v_mul_u32_u24_e32 v138, 0xfff8, v138
	v_add_u32_e32 v138, 0xffff0000, v138
	v_mov_b32_e32 v139, -1
	v_lshl_add_u64 v[134:135], v[54:55], 0, v[138:139]
	s_mov_b32 s28, 0x55555555
	s_mov_b32 s29, 0x55555555
	s_mov_b32 s30, 0xaaaaaaaa
	s_mov_b32 s31, 0xaaaaaaaa
	v_or_b32_e32 v1, v1, v121
	v_lshlrev_b32_e32 v4, 7, v120
	s_movk_i32 s12, 0x120
	v_mad_u32_u24 v1, v1, s12, v4
	s_add_u32 s12, s10, 0x800000
	v_accvgpr_read_b32 v7, a72
	v_mov_b64_e32 v[80:81], v[28:29]
	s_addc_u32 s13, s11, 0
	v_lshlrev_b64 v[28:29], 2, v[94:95]
	v_readfirstlane_b32 s14, v7
	v_add_u32_e32 v7, 0, v90
	v_lshl_add_u64 v[4:5], s[12:13], 0, v[28:29]
	s_mov_b32 m0, s14
	v_lshlrev_b64 v[30:31], 2, v[96:97]
	v_readfirstlane_b32 s14, v7
	v_mov_b32_e32 v14, v7
	v_add_u32_e32 v7, 0, v91
	s_waitcnt lgkmcnt(0)
	v_lshlrev_b64 v[56:57], 2, v[98:99]
	v_mov_b32_e32 v19, v7
	v_lshlrev_b64 v[58:59], 2, v[100:101]
	v_add_u32_e32 v7, 0, v119
	v_accvgpr_read_b32 v25, a72
	v_mov_b32_e32 v21, v7
	v_lshl_add_u32 v15, v93, 3, v1
	v_add_u32_e32 v1, v1, v11
	s_waitcnt vmcnt(16)
	v_accvgpr_write_b32 a12, v14
	v_mov_b64_e32 v[124:125], v[56:57]
	v_accvgpr_write_b32 a13, v19
	v_mov_b64_e32 v[126:127], v[58:59]
	v_accvgpr_write_b32 a16, v21
	s_waitcnt lgkmcnt(0)
	s_barrier
	v_add_u32_e32 v14, 0x16010, v15
	v_mov_b32_e32 v122, v15
	v_add_u32_e32 v15, 0x16000, v1
	ds_read_b64 v[64:65], v14
	ds_read_b64 v[66:67], v14 offset:288
	ds_read_b64 v[68:69], v14 offset:576
	ds_read_b64 v[76:77], v14 offset:1728
	ds_read_b64 v[78:79], v14 offset:2016
	ds_read_b64 v[4:5], v14 offset:2304
	ds_read_b64 v[84:85], v14 offset:3456
	ds_read_b64 v[74:75], v14 offset:3744
	ds_read_b64 v[88:89], v14 offset:4032
	ds_read_b64 v[100:101], v14 offset:5184
	ds_read_b64 v[106:107], v14 offset:5472
	ds_read_b64 v[120:121], v14 offset:5760
	ds_read_b32 v43, v15
	ds_read_b32 v19, v15 offset:288
	ds_read_b32 v39, v15 offset:576
	ds_read_b32 v25, v15 offset:1728
	ds_read_b32 v7, v15 offset:2016
	ds_read_b32 v21, v15 offset:2304
	ds_read_b32 v11, v15 offset:3456
	ds_read_b32 v35, v15 offset:3744
	ds_read_b32 v59, v15 offset:4032
	ds_read_b32 v57, v15 offset:5184
	ds_read_b32 v51, v15 offset:5472
	ds_read_b32 v49, v15 offset:5760
	s_waitcnt lgkmcnt(0)
	v_accvgpr_read_b32 v8, a26
	v_mov_b32_e32 v46, v43
	v_mov_b32_e32 v113, v65
	v_mov_b32_e32 v26, v19
	v_mov_b32_dpp v46, v65 row_shr:1 row_mask:0xf bank_mask:0xf
	v_pk_mul_f32 v[70:71], v[112:113], v[46:47]
	v_accvgpr_read_b32 v9, a22
	v_accvgpr_read_b32 v27, a36
	v_mov_b32_dpp v43, v64 row_shl:1 row_mask:0xf bank_mask:0xf
	v_mov_b32_dpp v26, v67 row_shr:1 row_mask:0xf bank_mask:0xf
	v_pk_fma_f32 v[70:71], v[64:65], v[116:117], v[70:71] op_sel_hi:[0,1,1]
	v_pk_mov_b32 v[64:65], v[64:65], v[86:87] op_sel:[1,0]
	v_mov_b32_e32 v17, v67
	v_mov_b64_e32 v[102:103], v[8:9]
	v_accvgpr_read_b32 v8, a25
	v_accvgpr_read_b32 v114, a24
	v_accvgpr_read_b32 v9, a21
	v_accvgpr_read_b32 v115, a20
	v_accvgpr_read_b32 v2, a32
	v_mov_b64_e32 v[82:83], v[30:31]
	v_pk_fma_f32 v[70:71], v[64:65], v[42:43], v[70:71]
	v_pk_mul_f32 v[64:65], v[16:17], v[26:27]
	v_mov_b64_e32 v[30:31], v[32:33]
	v_accvgpr_read_b32 v18, a44
	v_mov_b64_e32 v[104:105], v[8:9]
	v_cndmask_b32_e32 v9, 0, v2, vcc
	v_accvgpr_write_b32 a4, v14
	v_mov_b32_dpp v19, v66 row_shl:1 row_mask:0xf bank_mask:0xf
	v_pk_fma_f32 v[64:65], v[66:67], v[114:115], v[64:65] op_sel_hi:[0,1,1]
	v_pk_mov_b32 v[66:67], v[66:67], v[30:31] op_sel:[1,0]
	v_accvgpr_read_b32 v14, a69
	v_mov_b32_e32 v44, v39
	v_mov_b32_e32 v60, v1
	v_pk_fma_f32 v[66:67], v[66:67], v[18:19], v[64:65]
	v_cndmask_b32_e32 v14, 0, v14, vcc
	v_cndmask_b32_e64 v0, v9, 0, s[2:3]
	v_mov_b32_dpp v44, v69 row_shr:1 row_mask:0xf bank_mask:0xf
	v_pk_add_f32 v[70:71], v[70:71], 0 op_sel_hi:[1,0]
	v_mov_b32_e32 v1, v69
	v_accvgpr_write_b32 a0, v15
	v_cndmask_b32_e64 v15, v14, 0, s[4:5]
	v_cndmask_b32_e64 v14, v12, 0, s[4:5]
	v_pk_add_f32 v[66:67], v[70:71], v[66:67]
	v_pk_mul_f32 v[70:71], v[0:1], v[44:45]
	v_mov_b32_dpp v39, v68 row_shl:1 row_mask:0xf bank_mask:0xf
	v_pk_fma_f32 v[70:71], v[68:69], v[80:81], v[70:71] op_sel_hi:[0,1,1]
	v_pk_mov_b32 v[68:69], v[68:69], v[14:15] op_sel:[1,0]
	v_accvgpr_read_b32 v9, a1
	v_pk_fma_f32 v[68:69], v[68:69], v[38:39], v[70:71]
	v_mov_b32_e32 v36, v25
	v_cndmask_b32_e64 v64, v9, 0, s[8:9]
	v_pk_add_f32 v[66:67], v[66:67], v[68:69]
	v_mov_b32_dpp v36, v77 row_shr:1 row_mask:0xf bank_mask:0xf
	v_mov_b32_e32 v65, v77
	v_mov_b64_e32 v[108:109], v[22:23]
	v_accvgpr_read_b32 v9, a9
	v_mov_b32_e32 v128, v66
	v_mov_b32_e32 v129, v67
	v_mov_b32_e32 v12, v7
	v_pk_mul_f32 v[66:67], v[64:65], v[36:37]
	v_accvgpr_read_b32 v13, a37
	v_mov_b64_e32 v[72:73], v[28:29]
	v_cndmask_b32_e64 v28, v9, 0, s[2:3]
	v_mov_b32_dpp v25, v76 row_shl:1 row_mask:0xf bank_mask:0xf
	v_mov_b32_dpp v12, v79 row_shr:1 row_mask:0xf bank_mask:0xf
	v_pk_fma_f32 v[66:67], v[76:77], v[108:109], v[66:67] op_sel_hi:[0,1,1]
	v_mov_b32_e32 v76, v77
	v_mov_b32_e32 v77, v87
	v_mov_b32_e32 v29, v79
	v_pk_fma_f32 v[66:67], v[76:77], v[24:25], v[66:67]
	v_pk_mul_f32 v[76:77], v[28:29], v[12:13]
	v_accvgpr_read_b32 v6, a45
	v_accvgpr_read_b32 v2, a33
	v_mov_b32_dpp v7, v78 row_shl:1 row_mask:0xf bank_mask:0xf
	v_pk_fma_f32 v[76:77], v[78:79], v[104:105], v[76:77] op_sel_hi:[0,1,1]
	v_mov_b32_e32 v78, v79
	v_mov_b32_e32 v79, v31
	v_cndmask_b32_e32 v2, 0, v2, vcc
	v_accvgpr_read_b32 v50, a53
	v_pk_fma_f32 v[76:77], v[78:79], v[6:7], v[76:77]
	v_mov_b32_e32 v78, v21
	v_accvgpr_write_b32 a44, v80
	v_cndmask_b32_e32 v79, 0, v50, vcc
	v_cndmask_b32_e64 v52, v2, 0, s[2:3]
	v_mov_b32_dpp v78, v5 row_shr:1 row_mask:0xf bank_mask:0xf
	v_pk_add_f32 v[66:67], v[66:67], 0 op_sel_hi:[1,0]
	v_mov_b32_e32 v53, v5
	v_accvgpr_write_b32 a45, v81
	v_accvgpr_write_b32 a21, v15
	v_pk_add_f32 v[80:81], v[66:67], v[76:77]
	v_pk_mul_f32 v[66:67], v[52:53], v[78:79]
	v_accvgpr_write_b32 a24, v40
	v_accvgpr_read_b32 v2, a2
	v_mov_b32_dpp v21, v4 row_shl:1 row_mask:0xf bank_mask:0xf
	v_pk_fma_f32 v[66:67], v[4:5], v[40:41], v[66:67] op_sel_hi:[0,1,1]
	v_accvgpr_write_b32 a25, v41
	v_mov_b32_e32 v4, v5
	v_accvgpr_read_b32 v5, a21
	v_cndmask_b32_e64 v40, v2, 0, s[8:9]
	v_accvgpr_read_b32 v2, a62
	v_accvgpr_read_b32 v8, a18
	v_accvgpr_read_b32 v48, a63
	v_accvgpr_write_b32 a20, v14
	v_accvgpr_write_b32 a41, v23
	v_pk_fma_f32 v[4:5], v[4:5], v[20:21], v[66:67]
	s_mov_b64 s[12:13], 0x10000
	v_cndmask_b32_e64 v14, v2, 0, s[6:7]
	v_mov_b32_e32 v76, v11
	v_accvgpr_read_b32 v2, a10
	v_accvgpr_write_b32 a40, v22
	v_cndmask_b32_e64 v15, v48, 0, s[6:7]
	v_cndmask_b32_e64 v77, v8, 0, s[0:1]
	v_pk_add_f32 v[4:5], v[80:81], v[4:5]
	v_lshl_add_u64 v[136:137], v[134:135], 0, s[12:13]
	v_mov_b32_dpp v76, v85 row_shr:1 row_mask:0xf bank_mask:0xf
	v_mov_b32_e32 v41, v85
	v_cndmask_b32_e64 v22, v2, 0, s[2:3]
	v_mov_b32_e32 v2, v35
	v_accvgpr_read_b32 v1, a50
	v_accvgpr_read_b32 v3, a38
	s_mov_b64 s[32:33], vcc
	s_nop 1
	s_mov_b64 vcc, s[28:29]
	s_nop 0
	v_cndmask_b32_dpp v130, v4, v128, vcc quad_perm:[1,0,3,2] row_mask:0xf bank_mask:0xf
	v_cndmask_b32_dpp v131, v5, v129, vcc quad_perm:[1,0,3,2] row_mask:0xf bank_mask:0xf
	s_mov_b64 vcc, s[30:31]
	s_nop 0
	v_cndmask_b32_dpp v132, v128, v4, vcc quad_perm:[1,0,3,2] row_mask:0xf bank_mask:0xf
	v_cndmask_b32_dpp v133, v129, v5, vcc quad_perm:[1,0,3,2] row_mask:0xf bank_mask:0xf
	global_store_dwordx4 v[136:137], v[130:133], off sc0 sc1 nt
	s_nop 1
	s_mov_b64 vcc, s[32:33]
	v_mov_b64_e32 v[8:9], v[14:15]
	v_pk_mul_f32 v[4:5], v[40:41], v[76:77]
	v_mov_b64_e32 v[66:67], v[62:63]
	v_mov_b32_dpp v2, v75 row_shr:1 row_mask:0xf bank_mask:0xf
	v_mov_b32_e32 v23, v75
	v_cndmask_b32_e32 v62, 0, v1, vcc
	v_accvgpr_read_b32 v1, a42
	v_mov_b32_dpp v11, v84 row_shl:1 row_mask:0xf bank_mask:0xf
	v_pk_fma_f32 v[4:5], v[84:85], v[66:67], v[4:5] op_sel_hi:[0,1,1]
	v_pk_mov_b32 v[80:81], v[84:85], v[8:9] op_sel:[1,0]
	v_pk_mul_f32 v[84:85], v[22:23], v[2:3]
	v_accvgpr_read_b32 v2, a58
	v_cndmask_b32_e32 v63, 0, v1, vcc
	v_accvgpr_read_b32 v1, a70
	v_pk_fma_f32 v[80:81], v[80:81], v[10:11], v[4:5]
	v_accvgpr_read_b32 v4, a66
	v_cndmask_b32_e32 v58, 0, v2, vcc
	v_cndmask_b32_e32 v1, 0, v1, vcc
	v_accvgpr_read_b32 v2, a71
	v_cndmask_b32_e64 v8, v4, 0, s[4:5]
	v_cndmask_b32_e32 v2, 0, v2, vcc
	v_cndmask_b32_e64 v4, v1, 0, s[4:5]
	v_accvgpr_read_b32 v1, a34
	v_mov_b32_e32 v9, v61
	v_cndmask_b32_e64 v5, v2, 0, s[4:5]
	v_cndmask_b32_e32 v1, 0, v1, vcc
	v_accvgpr_read_b32 v2, a54
	v_mov_b32_e32 v92, v59
	v_accvgpr_read_b32 v34, a46
	v_mov_b32_dpp v35, v74 row_shl:1 row_mask:0xf bank_mask:0xf
	v_pk_fma_f32 v[84:85], v[74:75], v[102:103], v[84:85] op_sel_hi:[0,1,1]
	v_pk_mov_b32 v[74:75], v[74:75], v[8:9] op_sel:[1,0]
	v_cndmask_b32_e32 v93, 0, v2, vcc
	v_mov_b32_dpp v92, v89 row_shr:1 row_mask:0xf bank_mask:0xf
	v_cndmask_b32_e64 v96, v1, 0, s[2:3]
	v_mov_b32_e32 v97, v89
	v_accvgpr_read_b32 v1, a31
	v_pk_fma_f32 v[74:75], v[74:75], v[34:35], v[84:85]
	v_pk_mul_f32 v[84:85], v[96:97], v[92:93]
	v_accvgpr_write_b32 a8, v62
	v_cndmask_b32_e64 v56, v1, 0, s[0:1]
	v_accvgpr_read_b32 v1, a15
	v_pk_fma_f32 v[84:85], v[88:89], v[62:63], v[84:85] op_sel_hi:[0,1,1]
	v_accvgpr_write_b32 a9, v63
	v_cndmask_b32_e64 v62, v1, 0, s[0:1]
	v_accvgpr_read_b32 v1, a7
	v_cndmask_b32_e64 v63, v1, 0, s[0:1]
	v_accvgpr_read_b32 v1, a19
	v_pk_add_f32 v[80:81], v[80:81], 0 op_sel_hi:[1,0]
	v_mov_b32_dpp v59, v88 row_shl:1 row_mask:0xf bank_mask:0xf
	v_pk_mov_b32 v[88:89], v[88:89], v[4:5] op_sel:[1,0]
	v_cndmask_b32_e64 v95, v1, 0, s[0:1]
	v_accvgpr_read_b32 v1, a3
	v_accvgpr_write_b32 a36, v104
	v_pk_add_f32 v[80:81], v[80:81], v[74:75]
	v_pk_fma_f32 v[84:85], v[88:89], v[58:59], v[84:85]
	v_mov_b32_e32 v94, v57
	v_cndmask_b32_e64 v98, v1, 0, s[8:9]
	v_accvgpr_read_b32 v1, a11
	v_accvgpr_write_b32 a37, v105
	v_accvgpr_write_b32 a32, v102
	v_pk_add_f32 v[80:81], v[80:81], v[84:85]
	s_mov_b64 s[4:5], 0x20000
	v_mov_b32_dpp v94, v101 row_shr:1 row_mask:0xf bank_mask:0xf
	v_mov_b32_e32 v99, v101
	v_cndmask_b32_e64 v104, v1, 0, s[2:3]
	v_accvgpr_read_b32 v1, a59
	v_accvgpr_write_b32 a29, v15
	v_accvgpr_write_b32 a33, v103
	v_accvgpr_write_b32 a49, v5
	v_lshl_add_u64 v[84:85], v[54:55], 0, s[4:5]
	v_mov_b32_e32 v128, v80
	v_mov_b32_e32 v129, v81
	v_pk_mul_f32 v[80:81], v[98:99], v[94:95]
	v_mov_b32_e32 v102, v51
	v_cndmask_b32_e32 v48, 0, v1, vcc
	v_accvgpr_read_b32 v1, a51
	v_accvgpr_write_b32 a48, v4
	v_mov_b32_dpp v57, v100 row_shl:1 row_mask:0xf bank_mask:0xf
	v_pk_fma_f32 v[80:81], v[100:101], v[62:63], v[80:81] op_sel_hi:[0,1,1]
	v_mov_b32_e32 v84, v101
	v_accvgpr_read_b32 v85, a29
	v_accvgpr_read_b32 v103, a39
	v_mov_b32_dpp v102, v107 row_shr:1 row_mask:0xf bank_mask:0xf
	v_mov_b32_e32 v105, v107
	v_cndmask_b32_e32 v4, 0, v1, vcc
	v_accvgpr_read_b32 v1, a43
	v_pk_fma_f32 v[80:81], v[84:85], v[56:57], v[80:81]
	v_accvgpr_read_b32 v30, a27
	v_accvgpr_read_b32 v31, a23
	v_pk_mul_f32 v[84:85], v[104:105], v[102:103]
	v_cndmask_b32_e32 v5, 0, v1, vcc
	v_accvgpr_read_b32 v1, a35
	v_accvgpr_read_b32 v50, a47
	v_mov_b32_dpp v51, v106 row_shl:1 row_mask:0xf bank_mask:0xf
	v_pk_fma_f32 v[84:85], v[106:107], v[30:31], v[84:85] op_sel_hi:[0,1,1]
	v_mov_b32_e32 v106, v107
	v_mov_b32_e32 v107, v9
	v_cndmask_b32_e32 v1, 0, v1, vcc
	v_accvgpr_read_b32 v2, a55
	v_mov_b32_e32 v108, v49
	v_pk_fma_f32 v[84:85], v[106:107], v[50:51], v[84:85]
	v_pk_add_f32 v[80:81], v[80:81], 0 op_sel_hi:[1,0]
	v_cndmask_b32_e32 v109, 0, v2, vcc
	v_mov_b32_dpp v108, v121 row_shr:1 row_mask:0xf bank_mask:0xf
	v_cndmask_b32_e64 v110, v1, 0, s[2:3]
	v_mov_b32_e32 v111, v121
	v_pk_add_f32 v[80:81], v[80:81], v[84:85]
	v_pk_mul_f32 v[84:85], v[110:111], v[108:109]
	v_mov_b32_dpp v49, v120 row_shl:1 row_mask:0xf bank_mask:0xf
	v_pk_fma_f32 v[84:85], v[120:121], v[4:5], v[84:85] op_sel_hi:[0,1,1]
	v_mov_b32_e32 v120, v121
	v_accvgpr_read_b32 v121, a49
	v_pk_fma_f32 v[84:85], v[120:121], v[48:49], v[84:85]
	s_mov_b64 s[0:1], 0x30000
	v_pk_add_f32 v[80:81], v[80:81], v[84:85]
	v_lshl_add_u64 v[136:137], v[134:135], 0, s[0:1]
	v_add_u32_e32 v1, s17, v118
	s_add_u32 s0, s10, 0x1400000
	s_mov_b64 s[32:33], vcc
	s_nop 1
	s_mov_b64 vcc, s[28:29]
	s_nop 0
	v_cndmask_b32_dpp v130, v80, v128, vcc quad_perm:[1,0,3,2] row_mask:0xf bank_mask:0xf
	v_cndmask_b32_dpp v131, v81, v129, vcc quad_perm:[1,0,3,2] row_mask:0xf bank_mask:0xf
	s_mov_b64 vcc, s[30:31]
	s_nop 0
	v_cndmask_b32_dpp v132, v128, v80, vcc quad_perm:[1,0,3,2] row_mask:0xf bank_mask:0xf
	v_cndmask_b32_dpp v133, v129, v81, vcc quad_perm:[1,0,3,2] row_mask:0xf bank_mask:0xf
	global_store_dwordx4 v[136:137], v[130:133], off sc0 sc1 nt
	s_nop 1
	s_mov_b64 vcc, s[32:33]
	v_readfirstlane_b32 s2, v1
	s_addc_u32 s1, s11, 0
	v_add_u32_e32 v1, s17, v90
	s_waitcnt vmcnt(12)
	v_lshl_add_u64 v[80:81], s[0:1], 0, v[72:73]
	s_mov_b32 m0, s2
	v_readfirstlane_b32 s2, v1
	v_mov_b64_e32 v[74:75], v[82:83]
	v_add_u32_e32 v1, s17, v91
	s_waitcnt lgkmcnt(0)
	s_barrier
	global_load_lds_dwordx4 v[80:81], off nt
	v_lshl_add_u64 v[80:81], s[0:1], 0, v[74:75]
	s_mov_b32 m0, s2
	v_readfirstlane_b32 s2, v1
	v_add_u32_e32 v1, s17, v119
	global_load_lds_dwordx4 v[80:81], off nt
	v_lshl_add_u64 v[80:81], s[0:1], 0, v[124:125]
	s_mov_b32 m0, s2
	v_readfirstlane_b32 s2, v1
	global_load_lds_dwordx4 v[80:81], off nt
	v_lshl_add_u64 v[80:81], s[0:1], 0, v[126:127]
	s_mov_b32 m0, s2
	v_accvgpr_write_b32 a53, v33
	v_accvgpr_write_b32 a2, v62
	v_accvgpr_write_b32 a7, v5
	v_accvgpr_write_b32 a22, v124
	v_accvgpr_write_b32 a30, v126
	global_load_lds_dwordx4 v[80:81], off nt
	v_accvgpr_write_b32 a52, v32
	v_accvgpr_write_b32 a3, v63
	v_accvgpr_write_b32 a6, v4
	v_mov_b64_e32 v[32:33], v[72:73]
	v_accvgpr_write_b32 a23, v125
	v_accvgpr_write_b32 a31, v127
	v_add_u32_e32 v2, 0x1d010, v122
	v_accvgpr_write_b32 a10, v122
	v_add_u32_e32 v5, 0x1d000, v60
	v_mov_b32_e32 v4, v60
	ds_read_b64 v[62:63], v2
	ds_read_b64 v[60:61], v2 offset:288
	ds_read_b64 v[72:73], v2 offset:576
	ds_read_b64 v[70:71], v2 offset:1728
	ds_read_b64 v[68:69], v2 offset:2016
	ds_read_b64 v[82:83], v2 offset:2304
	ds_read_b64 v[80:81], v2 offset:3456
	ds_read_b64 v[84:85], v2 offset:3744
	ds_read_b64 v[126:127], v2 offset:4032
	ds_read_b64 v[124:125], v2 offset:5184
	ds_read_b64 v[122:123], v2 offset:5472
	ds_read_b64 v[120:121], v2 offset:5760
	ds_read_b32 v43, v5
	ds_read_b32 v19, v5 offset:288
	ds_read_b32 v39, v5 offset:576
	ds_read_b32 v25, v5 offset:1728
	ds_read_b32 v7, v5 offset:2016
	ds_read_b32 v21, v5 offset:2304
	ds_read_b32 v11, v5 offset:3456
	ds_read_b32 v35, v5 offset:3744
	ds_read_b32 v59, v5 offset:4032
	ds_read_b32 v57, v5 offset:5184
	ds_read_b32 v51, v5 offset:5472
	ds_read_b32 v49, v5 offset:5760
	s_waitcnt lgkmcnt(0)
	v_mov_b64_e32 v[100:101], v[86:87]
	v_mov_b32_e32 v46, v43
	v_mov_b32_e32 v113, v63
	v_mov_b32_e32 v26, v19
	v_mov_b32_dpp v46, v63 row_shr:1 row_mask:0xf bank_mask:0xf
	v_pk_mul_f32 v[88:89], v[112:113], v[46:47]
	v_mov_b32_dpp v43, v62 row_shl:1 row_mask:0xf bank_mask:0xf
	v_pk_fma_f32 v[88:89], v[62:63], v[116:117], v[88:89] op_sel_hi:[0,1,1]
	v_pk_mov_b32 v[62:63], v[62:63], v[100:101] op_sel:[1,0]
	v_mov_b32_dpp v26, v61 row_shr:1 row_mask:0xf bank_mask:0xf
	v_mov_b32_e32 v17, v61
	v_pk_fma_f32 v[62:63], v[62:63], v[42:43], v[88:89]
	v_pk_mul_f32 v[88:89], v[16:17], v[26:27]
	v_accvgpr_write_b32 a34, v16
	v_accvgpr_read_b32 v16, a52
	v_accvgpr_read_b32 v17, a53
	v_mov_b32_dpp v19, v60 row_shl:1 row_mask:0xf bank_mask:0xf
	v_pk_fma_f32 v[88:89], v[60:61], v[114:115], v[88:89] op_sel_hi:[0,1,1]
	v_pk_mov_b32 v[60:61], v[60:61], v[16:17] op_sel:[1,0]
	v_mov_b32_e32 v44, v39
	v_accvgpr_write_b32 a28, v14
	v_pk_fma_f32 v[60:61], v[60:61], v[18:19], v[88:89]
	v_pk_add_f32 v[62:63], v[62:63], 0 op_sel_hi:[1,0]
	v_mov_b32_dpp v44, v73 row_shr:1 row_mask:0xf bank_mask:0xf
	v_mov_b32_e32 v1, v73
	v_accvgpr_read_b32 v14, a44
	v_accvgpr_read_b32 v89, a21
	v_pk_add_f32 v[60:61], v[62:63], v[60:61]
	v_pk_mul_f32 v[62:63], v[0:1], v[44:45]
	v_accvgpr_read_b32 v15, a45
	v_accvgpr_read_b32 v88, a20
	v_mov_b32_dpp v39, v72 row_shl:1 row_mask:0xf bank_mask:0xf
	v_pk_fma_f32 v[62:63], v[72:73], v[14:15], v[62:63] op_sel_hi:[0,1,1]
	v_pk_mov_b32 v[72:73], v[72:73], v[88:89] op_sel:[1,0]
	v_mov_b32_e32 v36, v25
	v_pk_fma_f32 v[62:63], v[72:73], v[38:39], v[62:63]
	s_mov_b64 s[0:1], 0x400000
	v_pk_add_f32 v[60:61], v[60:61], v[62:63]
	v_mov_b32_dpp v36, v71 row_shr:1 row_mask:0xf bank_mask:0xf
	v_mov_b32_e32 v65, v71
	v_accvgpr_read_b32 v87, a41
	v_lshl_add_u64 v[62:63], v[54:55], 0, s[0:1]
	v_mov_b32_e32 v128, v60
	v_mov_b32_e32 v129, v61
	v_pk_mul_f32 v[60:61], v[64:65], v[36:37]
	v_accvgpr_read_b32 v86, a40
	v_mov_b32_e32 v12, v7
	v_mov_b32_dpp v25, v70 row_shl:1 row_mask:0xf bank_mask:0xf
	v_pk_fma_f32 v[60:61], v[70:71], v[86:87], v[60:61] op_sel_hi:[0,1,1]
	v_mov_b32_e32 v62, v71
	v_mov_b32_e32 v63, v101
	v_mov_b32_dpp v12, v69 row_shr:1 row_mask:0xf bank_mask:0xf
	v_mov_b32_e32 v29, v69
	v_accvgpr_read_b32 v107, a37
	v_pk_fma_f32 v[60:61], v[62:63], v[24:25], v[60:61]
	v_pk_mul_f32 v[62:63], v[28:29], v[12:13]
	v_accvgpr_read_b32 v106, a36
	v_mov_b32_dpp v7, v68 row_shl:1 row_mask:0xf bank_mask:0xf
	v_pk_fma_f32 v[62:63], v[68:69], v[106:107], v[62:63] op_sel_hi:[0,1,1]
	v_mov_b32_e32 v68, v69
	v_mov_b32_e32 v69, v17
	v_mov_b32_e32 v78, v21
	v_pk_fma_f32 v[62:63], v[68:69], v[6:7], v[62:63]
	v_pk_add_f32 v[60:61], v[60:61], 0 op_sel_hi:[1,0]
	v_mov_b32_dpp v78, v83 row_shr:1 row_mask:0xf bank_mask:0xf
	v_mov_b32_e32 v53, v83
	v_accvgpr_read_b32 v14, a24
	v_pk_add_f32 v[60:61], v[60:61], v[62:63]
	v_pk_mul_f32 v[62:63], v[52:53], v[78:79]
	v_accvgpr_read_b32 v15, a25
	v_mov_b32_dpp v21, v82 row_shl:1 row_mask:0xf bank_mask:0xf
	v_pk_fma_f32 v[62:63], v[82:83], v[14:15], v[62:63] op_sel_hi:[0,1,1]
	v_mov_b32_e32 v68, v83
	v_mov_b32_e32 v69, v89
	v_pk_fma_f32 v[62:63], v[68:69], v[20:21], v[62:63]
	v_mov_b32_e32 v76, v11
	v_pk_add_f32 v[60:61], v[60:61], v[62:63]
	s_mov_b64 s[0:1], 0x410000
	v_mov_b32_dpp v76, v81 row_shr:1 row_mask:0xf bank_mask:0xf
	v_mov_b32_e32 v41, v81
	v_lshl_add_u64 v[136:137], v[134:135], 0, s[0:1]
	s_nop 1
	s_mov_b64 vcc, s[28:29]
	s_nop 0
	v_cndmask_b32_dpp v130, v60, v128, vcc quad_perm:[1,0,3,2] row_mask:0xf bank_mask:0xf
	v_cndmask_b32_dpp v131, v61, v129, vcc quad_perm:[1,0,3,2] row_mask:0xf bank_mask:0xf
	s_mov_b64 vcc, s[30:31]
	s_nop 0
	v_cndmask_b32_dpp v132, v128, v60, vcc quad_perm:[1,0,3,2] row_mask:0xf bank_mask:0xf
	v_cndmask_b32_dpp v133, v129, v61, vcc quad_perm:[1,0,3,2] row_mask:0xf bank_mask:0xf
	global_store_dwordx4 v[136:137], v[130:133], off sc0 sc1 nt
	s_nop 1
	v_pk_mul_f32 v[60:61], v[40:41], v[76:77]
	v_accvgpr_write_b32 a36, v66
	v_pk_fma_f32 v[60:61], v[80:81], v[66:67], v[60:61] op_sel_hi:[0,1,1]
	v_accvgpr_write_b32 a37, v67
	v_accvgpr_read_b32 v67, a29
	v_accvgpr_write_b32 a5, v2
	v_accvgpr_write_b32 a38, v100
	v_accvgpr_read_b32 v66, a28
	v_mov_b32_e32 v2, v35
	v_accvgpr_write_b32 a39, v101
	v_mov_b32_dpp v11, v80 row_shl:1 row_mask:0xf bank_mask:0xf
	v_pk_mov_b32 v[62:63], v[80:81], v[66:67] op_sel:[1,0]
	v_mov_b32_dpp v2, v85 row_shr:1 row_mask:0xf bank_mask:0xf
	v_mov_b32_e32 v23, v85
	v_accvgpr_read_b32 v101, a33
	v_pk_fma_f32 v[60:61], v[62:63], v[10:11], v[60:61]
	v_pk_mul_f32 v[62:63], v[22:23], v[2:3]
	v_accvgpr_read_b32 v100, a32
	v_mov_b32_dpp v35, v84 row_shl:1 row_mask:0xf bank_mask:0xf
	v_pk_fma_f32 v[62:63], v[84:85], v[100:101], v[62:63] op_sel_hi:[0,1,1]
	v_pk_mov_b32 v[68:69], v[84:85], v[8:9] op_sel:[1,0]
	v_mov_b32_e32 v92, v59
	v_pk_fma_f32 v[62:63], v[68:69], v[34:35], v[62:63]
	v_pk_add_f32 v[60:61], v[60:61], 0 op_sel_hi:[1,0]
	v_mov_b32_dpp v92, v127 row_shr:1 row_mask:0xf bank_mask:0xf
	v_mov_b32_e32 v97, v127
	v_accvgpr_read_b32 v17, a9
	v_accvgpr_read_b32 v71, a49
	v_pk_add_f32 v[60:61], v[60:61], v[62:63]
	v_pk_mul_f32 v[62:63], v[96:97], v[92:93]
	v_accvgpr_read_b32 v16, a8
	v_accvgpr_read_b32 v70, a48
	v_mov_b32_dpp v59, v126 row_shl:1 row_mask:0xf bank_mask:0xf
	v_pk_fma_f32 v[62:63], v[126:127], v[16:17], v[62:63] op_sel_hi:[0,1,1]
	v_pk_mov_b32 v[68:69], v[126:127], v[70:71] op_sel:[1,0]
	v_mov_b32_e32 v94, v57
	v_pk_fma_f32 v[62:63], v[68:69], v[58:59], v[62:63]
	v_accvgpr_write_b32 a20, v28
	v_pk_add_f32 v[60:61], v[60:61], v[62:63]
	s_mov_b64 s[0:1], 0x420000
	v_mov_b32_dpp v94, v125 row_shr:1 row_mask:0xf bank_mask:0xf
	v_mov_b32_e32 v99, v125
	v_accvgpr_read_b32 v29, a3
	v_lshl_add_u64 v[62:63], v[54:55], 0, s[0:1]
	v_mov_b32_e32 v128, v60
	v_mov_b32_e32 v129, v61
	v_pk_mul_f32 v[60:61], v[98:99], v[94:95]
	v_accvgpr_read_b32 v28, a2
	v_mov_b32_e32 v102, v51
	v_mov_b32_dpp v57, v124 row_shl:1 row_mask:0xf bank_mask:0xf
	v_pk_fma_f32 v[60:61], v[124:125], v[28:29], v[60:61] op_sel_hi:[0,1,1]
	v_mov_b32_e32 v62, v125
	v_mov_b32_e32 v63, v67
	v_mov_b32_dpp v102, v123 row_shr:1 row_mask:0xf bank_mask:0xf
	v_mov_b32_e32 v105, v123
	v_pk_fma_f32 v[60:61], v[62:63], v[56:57], v[60:61]
	v_pk_mul_f32 v[62:63], v[104:105], v[102:103]
	v_mov_b32_dpp v51, v122 row_shl:1 row_mask:0xf bank_mask:0xf
	v_pk_fma_f32 v[62:63], v[122:123], v[30:31], v[62:63] op_sel_hi:[0,1,1]
	v_accvgpr_write_b32 a28, v30
	v_mov_b32_e32 v68, v123
	v_mov_b32_e32 v69, v9
	v_mov_b32_e32 v108, v49
	v_accvgpr_write_b32 a29, v31
	v_pk_fma_f32 v[62:63], v[68:69], v[50:51], v[62:63]
	v_pk_add_f32 v[60:61], v[60:61], 0 op_sel_hi:[1,0]
	v_mov_b32_dpp v108, v121 row_shr:1 row_mask:0xf bank_mask:0xf
	v_mov_b32_e32 v111, v121
	v_accvgpr_read_b32 v31, a7
	v_pk_add_f32 v[60:61], v[60:61], v[62:63]
	v_pk_mul_f32 v[62:63], v[110:111], v[108:109]
	v_accvgpr_read_b32 v30, a6
	v_mov_b32_dpp v49, v120 row_shl:1 row_mask:0xf bank_mask:0xf
	v_pk_fma_f32 v[62:63], v[120:121], v[30:31], v[62:63] op_sel_hi:[0,1,1]
	v_mov_b32_e32 v68, v121
	v_mov_b32_e32 v69, v71
	v_pk_fma_f32 v[62:63], v[68:69], v[48:49], v[62:63]
	s_mov_b64 s[0:1], 0x430000
	v_pk_add_f32 v[60:61], v[60:61], v[62:63]
	v_lshl_add_u64 v[136:137], v[134:135], 0, s[0:1]
	v_add_u32_e32 v1, s16, v118
	s_add_u32 s0, s10, 0x1800000
	v_accvgpr_write_b32 a26, v114
	s_nop 1
	s_mov_b64 vcc, s[28:29]
	s_nop 0
	v_cndmask_b32_dpp v130, v60, v128, vcc quad_perm:[1,0,3,2] row_mask:0xf bank_mask:0xf
	v_cndmask_b32_dpp v131, v61, v129, vcc quad_perm:[1,0,3,2] row_mask:0xf bank_mask:0xf
	s_mov_b64 vcc, s[30:31]
	s_nop 0
	v_cndmask_b32_dpp v132, v128, v60, vcc quad_perm:[1,0,3,2] row_mask:0xf bank_mask:0xf
	v_cndmask_b32_dpp v133, v129, v61, vcc quad_perm:[1,0,3,2] row_mask:0xf bank_mask:0xf
	global_store_dwordx4 v[136:137], v[130:133], off sc0 sc1 nt
	s_nop 1
	v_readfirstlane_b32 s2, v1
	s_addc_u32 s1, s11, 0
	v_add_u32_e32 v1, s16, v90
	v_accvgpr_write_b32 a18, v116
	v_accvgpr_write_b32 a27, v115
	s_waitcnt vmcnt(16)
	v_lshl_add_u64 v[60:61], s[0:1], 0, v[32:33]
	s_mov_b32 m0, s2
	v_readfirstlane_b32 s2, v1
	v_add_u32_e32 v1, s16, v91
	v_accvgpr_read_b32 v115, a23
	v_accvgpr_write_b32 a19, v117
	s_waitcnt lgkmcnt(0)
	s_barrier
	global_load_lds_dwordx4 v[60:61], off nt
	v_lshl_add_u64 v[60:61], s[0:1], 0, v[74:75]
	s_mov_b32 m0, s2
	v_readfirstlane_b32 s2, v1
	v_accvgpr_read_b32 v114, a22
	v_add_u32_e32 v1, s16, v119
	v_accvgpr_read_b32 v117, a31
	global_load_lds_dwordx4 v[60:61], off nt
	v_lshl_add_u64 v[60:61], s[0:1], 0, v[114:115]
	s_mov_b32 m0, s2
	v_readfirstlane_b32 s2, v1
	v_accvgpr_read_b32 v116, a30
	global_load_lds_dwordx4 v[60:61], off nt
	v_lshl_add_u64 v[60:61], s[0:1], 0, v[116:117]
	s_mov_b32 m0, s2
	v_accvgpr_write_b32 a1, v5
	global_load_lds_dwordx4 v[60:61], off nt
	v_accvgpr_read_b32 v5, a10
	v_add_u32_e32 v2, 16, v5
	ds_read_b64 v[60:61], v2
	ds_read_b64 v[62:63], v2 offset:288
	ds_read_b64 v[68:69], v2 offset:576
	ds_read_b64 v[70:71], v2 offset:1728
	ds_read_b64 v[72:73], v2 offset:2016
	ds_read_b64 v[82:83], v2 offset:2304
	ds_read_b64 v[80:81], v2 offset:3456
	ds_read_b64 v[84:85], v2 offset:3744
	ds_read_b64 v[124:125], v2 offset:4032
	ds_read_b64 v[122:123], v2 offset:5184
	ds_read_b64 v[120:121], v2 offset:5472
	ds_read_b64 v[90:91], v2 offset:5760
	ds_read_b32 v43, v4
	ds_read_b32 v19, v4 offset:288
	ds_read_b32 v39, v4 offset:576
	ds_read_b32 v25, v4 offset:1728
	ds_read_b32 v7, v4 offset:2016
	ds_read_b32 v21, v4 offset:2304
	ds_read_b32 v11, v4 offset:3456
	ds_read_b32 v35, v4 offset:3744
	ds_read_b32 v59, v4 offset:4032
	ds_read_b32 v57, v4 offset:5184
	ds_read_b32 v51, v4 offset:5472
	ds_read_b32 v49, v4 offset:5760
	s_waitcnt lgkmcnt(0)
	v_accvgpr_write_b32 a46, v88
	v_mov_b32_e32 v46, v43
	v_accvgpr_write_b32 a8, v8
	v_mov_b32_e32 v113, v61
	v_mov_b32_dpp v46, v61 row_shr:1 row_mask:0xf bank_mask:0xf
	v_accvgpr_mov_b32 a42, a52
	v_accvgpr_write_b32 a47, v89
	v_accvgpr_write_b32 a9, v9
	v_pk_mul_f32 v[88:89], v[112:113], v[46:47]
	v_accvgpr_write_b32 a40, v112
	v_accvgpr_read_b32 v8, a18
	v_accvgpr_read_b32 v113, a39
	v_accvgpr_mov_b32 a43, a53
	v_accvgpr_write_b32 a51, v33
	v_accvgpr_write_b32 a52, v74
	v_accvgpr_read_b32 v9, a19
	v_accvgpr_read_b32 v112, a38
	v_mov_b32_e32 v26, v19
	v_accvgpr_write_b32 a50, v32
	v_accvgpr_write_b32 a53, v75
	v_mov_b32_dpp v43, v60 row_shl:1 row_mask:0xf bank_mask:0xf
	v_pk_fma_f32 v[88:89], v[60:61], v[8:9], v[88:89] op_sel_hi:[0,1,1]
	v_pk_mov_b32 v[60:61], v[60:61], v[112:113] op_sel:[1,0]
	v_mov_b32_dpp v26, v63 row_shr:1 row_mask:0xf bank_mask:0xf
	v_accvgpr_read_b32 v32, a34
	v_mov_b32_e32 v33, v63
	v_accvgpr_read_b32 v127, a27
	v_accvgpr_read_b32 v75, a43
	v_pk_fma_f32 v[60:61], v[60:61], v[42:43], v[88:89]
	v_pk_mul_f32 v[88:89], v[32:33], v[26:27]
	v_accvgpr_read_b32 v126, a26
	v_accvgpr_read_b32 v74, a42
	v_mov_b32_dpp v19, v62 row_shl:1 row_mask:0xf bank_mask:0xf
	v_pk_fma_f32 v[88:89], v[62:63], v[126:127], v[88:89] op_sel_hi:[0,1,1]
	v_pk_mov_b32 v[62:63], v[62:63], v[74:75] op_sel:[1,0]
	v_mov_b32_e32 v44, v39
	v_accvgpr_mov_b32 a14, a48
	v_pk_fma_f32 v[62:63], v[62:63], v[18:19], v[88:89]
	v_pk_add_f32 v[60:61], v[60:61], 0 op_sel_hi:[1,0]
	v_mov_b32_dpp v44, v69 row_shr:1 row_mask:0xf bank_mask:0xf
	v_mov_b32_e32 v1, v69
	v_accvgpr_mov_b32 a15, a49
	v_pk_add_f32 v[60:61], v[60:61], v[62:63]
	v_pk_mul_f32 v[62:63], v[0:1], v[44:45]
	v_accvgpr_write_b32 a48, v0
	v_accvgpr_read_b32 v89, a45
	v_accvgpr_read_b32 v0, a46
	v_accvgpr_read_b32 v88, a44
	v_accvgpr_read_b32 v1, a47
	v_mov_b32_dpp v39, v68 row_shl:1 row_mask:0xf bank_mask:0xf
	v_pk_fma_f32 v[62:63], v[68:69], v[88:89], v[62:63] op_sel_hi:[0,1,1]
	v_pk_mov_b32 v[68:69], v[68:69], v[0:1] op_sel:[1,0]
	v_mov_b32_e32 v36, v25
	v_pk_fma_f32 v[62:63], v[68:69], v[38:39], v[62:63]
	s_mov_b64 s[0:1], 0x800000
	v_pk_add_f32 v[60:61], v[60:61], v[62:63]
	v_mov_b32_dpp v36, v71 row_shr:1 row_mask:0xf bank_mask:0xf
	v_mov_b32_e32 v65, v71
	v_lshl_add_u64 v[62:63], v[54:55], 0, s[0:1]
	v_mov_b32_e32 v128, v60
	v_mov_b32_e32 v129, v61
	v_pk_mul_f32 v[60:61], v[64:65], v[36:37]
	v_mov_b64_e32 v[118:119], v[86:87]
	v_mov_b32_e32 v12, v7
	v_accvgpr_write_b32 a24, v32
	v_mov_b32_dpp v25, v70 row_shl:1 row_mask:0xf bank_mask:0xf
	v_pk_fma_f32 v[60:61], v[70:71], v[118:119], v[60:61] op_sel_hi:[0,1,1]
	v_mov_b32_e32 v62, v71
	v_mov_b32_e32 v63, v113
	v_mov_b32_dpp v12, v73 row_shr:1 row_mask:0xf bank_mask:0xf
	v_accvgpr_read_b32 v32, a20
	v_mov_b32_e32 v33, v73
	v_pk_fma_f32 v[60:61], v[62:63], v[24:25], v[60:61]
	v_pk_mul_f32 v[62:63], v[32:33], v[12:13]
	v_mov_b32_dpp v7, v72 row_shl:1 row_mask:0xf bank_mask:0xf
	v_pk_fma_f32 v[62:63], v[72:73], v[106:107], v[62:63] op_sel_hi:[0,1,1]
	v_mov_b32_e32 v68, v73
	v_mov_b32_e32 v69, v75
	v_mov_b32_e32 v78, v21
	v_pk_fma_f32 v[62:63], v[68:69], v[6:7], v[62:63]
	v_pk_add_f32 v[60:61], v[60:61], 0 op_sel_hi:[1,0]
	v_mov_b32_dpp v78, v83 row_shr:1 row_mask:0xf bank_mask:0xf
	v_mov_b32_e32 v53, v83
	v_pk_add_f32 v[60:61], v[60:61], v[62:63]
	v_pk_mul_f32 v[62:63], v[52:53], v[78:79]
	v_mov_b32_dpp v21, v82 row_shl:1 row_mask:0xf bank_mask:0xf
	v_pk_fma_f32 v[62:63], v[82:83], v[14:15], v[62:63] op_sel_hi:[0,1,1]
	v_mov_b32_e32 v68, v83
	v_mov_b32_e32 v69, v1
	v_accvgpr_write_b32 a19, v15
	v_pk_fma_f32 v[62:63], v[68:69], v[20:21], v[62:63]
	v_mov_b32_e32 v76, v11
	v_accvgpr_write_b32 a18, v14
	v_pk_add_f32 v[60:61], v[60:61], v[62:63]
	s_mov_b64 s[0:1], 0x810000
	v_mov_b32_dpp v76, v81 row_shr:1 row_mask:0xf bank_mask:0xf
	v_mov_b32_e32 v41, v81
	v_accvgpr_read_b32 v14, a36
	v_accvgpr_write_b32 a6, v2
	v_lshl_add_u64 v[136:137], v[134:135], 0, s[0:1]
	s_nop 1
	s_mov_b64 vcc, s[28:29]
	s_nop 0
	v_cndmask_b32_dpp v130, v60, v128, vcc quad_perm:[1,0,3,2] row_mask:0xf bank_mask:0xf
	v_cndmask_b32_dpp v131, v61, v129, vcc quad_perm:[1,0,3,2] row_mask:0xf bank_mask:0xf
	s_mov_b64 vcc, s[30:31]
	s_nop 0
	v_cndmask_b32_dpp v132, v128, v60, vcc quad_perm:[1,0,3,2] row_mask:0xf bank_mask:0xf
	v_cndmask_b32_dpp v133, v129, v61, vcc quad_perm:[1,0,3,2] row_mask:0xf bank_mask:0xf
	global_store_dwordx4 v[136:137], v[130:133], off sc0 sc1 nt
	s_nop 1
	v_pk_mul_f32 v[60:61], v[40:41], v[76:77]
	v_accvgpr_read_b32 v15, a37
	v_mov_b32_e32 v2, v35
	v_mov_b32_dpp v11, v80 row_shl:1 row_mask:0xf bank_mask:0xf
	v_pk_fma_f32 v[60:61], v[80:81], v[14:15], v[60:61] op_sel_hi:[0,1,1]
	v_pk_mov_b32 v[62:63], v[80:81], v[66:67] op_sel:[1,0]
	v_mov_b32_dpp v2, v85 row_shr:1 row_mask:0xf bank_mask:0xf
	v_mov_b32_e32 v23, v85
	v_accvgpr_read_b32 v15, a9
	v_pk_fma_f32 v[60:61], v[62:63], v[10:11], v[60:61]
	v_pk_mul_f32 v[62:63], v[22:23], v[2:3]
	v_accvgpr_read_b32 v14, a8
	v_mov_b32_dpp v35, v84 row_shl:1 row_mask:0xf bank_mask:0xf
	v_pk_fma_f32 v[62:63], v[84:85], v[100:101], v[62:63] op_sel_hi:[0,1,1]
	v_pk_mov_b32 v[68:69], v[84:85], v[14:15] op_sel:[1,0]
	v_mov_b32_e32 v92, v59
	v_pk_fma_f32 v[62:63], v[68:69], v[34:35], v[62:63]
	v_pk_add_f32 v[60:61], v[60:61], 0 op_sel_hi:[1,0]
	v_mov_b32_dpp v92, v125 row_shr:1 row_mask:0xf bank_mask:0xf
	v_mov_b32_e32 v97, v125
	v_accvgpr_read_b32 v71, a15
	v_pk_add_f32 v[60:61], v[60:61], v[62:63]
	v_pk_mul_f32 v[62:63], v[96:97], v[92:93]
	v_accvgpr_read_b32 v70, a14
	v_mov_b32_dpp v59, v124 row_shl:1 row_mask:0xf bank_mask:0xf
	v_pk_fma_f32 v[62:63], v[124:125], v[16:17], v[62:63] op_sel_hi:[0,1,1]
	v_pk_mov_b32 v[68:69], v[124:125], v[70:71] op_sel:[1,0]
	v_mov_b32_e32 v94, v57
	v_pk_fma_f32 v[62:63], v[68:69], v[58:59], v[62:63]
	s_mov_b64 s[0:1], 0x820000
	v_pk_add_f32 v[60:61], v[60:61], v[62:63]
	v_mov_b32_dpp v94, v123 row_shr:1 row_mask:0xf bank_mask:0xf
	v_mov_b32_e32 v99, v123
	v_accvgpr_write_b32 a31, v17
	v_lshl_add_u64 v[62:63], v[54:55], 0, s[0:1]
	v_mov_b32_e32 v128, v60
	v_mov_b32_e32 v129, v61
	v_pk_mul_f32 v[60:61], v[98:99], v[94:95]
	v_mov_b32_e32 v102, v51
	v_accvgpr_write_b32 a30, v16
	v_mov_b32_dpp v57, v122 row_shl:1 row_mask:0xf bank_mask:0xf
	v_pk_fma_f32 v[60:61], v[122:123], v[28:29], v[60:61] op_sel_hi:[0,1,1]
	v_mov_b32_e32 v62, v123
	v_mov_b32_e32 v63, v67
	v_mov_b32_dpp v102, v121 row_shr:1 row_mask:0xf bank_mask:0xf
	v_mov_b32_e32 v105, v121
	v_accvgpr_read_b32 v16, a28
	v_pk_fma_f32 v[60:61], v[62:63], v[56:57], v[60:61]
	v_pk_mul_f32 v[62:63], v[104:105], v[102:103]
	v_accvgpr_read_b32 v17, a29
	v_mov_b32_dpp v51, v120 row_shl:1 row_mask:0xf bank_mask:0xf
	v_pk_fma_f32 v[62:63], v[120:121], v[16:17], v[62:63] op_sel_hi:[0,1,1]
	v_mov_b32_e32 v68, v121
	v_mov_b32_e32 v69, v15
	v_mov_b32_e32 v108, v49
	v_pk_fma_f32 v[62:63], v[68:69], v[50:51], v[62:63]
	v_pk_add_f32 v[60:61], v[60:61], 0 op_sel_hi:[1,0]
	v_mov_b32_dpp v108, v91 row_shr:1 row_mask:0xf bank_mask:0xf
	v_mov_b32_e32 v111, v91
	v_pk_add_f32 v[60:61], v[60:61], v[62:63]
	v_pk_mul_f32 v[62:63], v[110:111], v[108:109]
	v_mov_b32_dpp v49, v90 row_shl:1 row_mask:0xf bank_mask:0xf
	v_pk_fma_f32 v[62:63], v[90:91], v[30:31], v[62:63] op_sel_hi:[0,1,1]
	v_mov_b32_e32 v68, v91
	v_mov_b32_e32 v69, v71
	v_pk_fma_f32 v[62:63], v[68:69], v[48:49], v[62:63]
	s_mov_b64 s[0:1], 0x830000
	v_mov_b32_e32 v0, v22
	v_pk_add_f32 v[60:61], v[60:61], v[62:63]
	v_lshl_add_u64 v[136:137], v[134:135], 0, s[0:1]
	s_add_u32 s0, s10, 0x1c00000
	v_accvgpr_read_b32 v22, a50
	v_accvgpr_read_b32 v1, a72
	s_addc_u32 s1, s11, 0
	v_accvgpr_read_b32 v23, a51
	s_nop 1
	s_mov_b64 vcc, s[28:29]
	s_nop 0
	v_cndmask_b32_dpp v130, v60, v128, vcc quad_perm:[1,0,3,2] row_mask:0xf bank_mask:0xf
	v_cndmask_b32_dpp v131, v61, v129, vcc quad_perm:[1,0,3,2] row_mask:0xf bank_mask:0xf
	s_mov_b64 vcc, s[30:31]
	s_nop 0
	v_cndmask_b32_dpp v132, v128, v60, vcc quad_perm:[1,0,3,2] row_mask:0xf bank_mask:0xf
	v_cndmask_b32_dpp v133, v129, v61, vcc quad_perm:[1,0,3,2] row_mask:0xf bank_mask:0xf
	global_store_dwordx4 v[136:137], v[130:133], off sc0 sc1 nt
	s_nop 1
	v_readfirstlane_b32 s2, v1
	v_lshl_add_u64 v[60:61], s[0:1], 0, v[22:23]
	v_accvgpr_read_b32 v1, a12
	v_accvgpr_read_b32 v22, a52
	s_waitcnt vmcnt(18)
	s_mov_b32 m0, s2
	v_readfirstlane_b32 s2, v1
	v_accvgpr_read_b32 v23, a53
	v_accvgpr_read_b32 v1, a13
	s_waitcnt lgkmcnt(0)
	s_barrier
	global_load_lds_dwordx4 v[60:61], off nt
	v_lshl_add_u64 v[60:61], s[0:1], 0, v[22:23]
	s_mov_b32 m0, s2
	v_readfirstlane_b32 s2, v1
	v_accvgpr_read_b32 v1, a16
	global_load_lds_dwordx4 v[60:61], off nt
	v_lshl_add_u64 v[60:61], s[0:1], 0, v[114:115]
	s_mov_b32 m0, s2
	v_readfirstlane_b32 s2, v1
	global_load_lds_dwordx4 v[60:61], off nt
	v_lshl_add_u64 v[60:61], s[0:1], 0, v[116:117]
	s_mov_b32 m0, s2
	v_accvgpr_write_b32 a22, v30
	v_accvgpr_write_b32 a44, v70
	global_load_lds_dwordx4 v[60:61], off nt
	v_accvgpr_write_b32 a2, v106
	v_accvgpr_write_b32 a34, v74
	v_accvgpr_write_b32 a23, v31
	v_accvgpr_write_b32 a45, v71
	v_add_u32_e32 v2, 0x7010, v5
	v_mov_b32_e32 v31, v5
	v_add_u32_e32 v5, 0x7000, v4
	ds_read_b64 v[60:61], v2
	ds_read_b64 v[62:63], v2 offset:288
	ds_read_b64 v[68:69], v2 offset:576
	ds_read_b64 v[70:71], v2 offset:1728
	ds_read_b64 v[72:73], v2 offset:2016
	ds_read_b64 v[82:83], v2 offset:2304
	ds_read_b64 v[80:81], v2 offset:3456
	ds_read_b64 v[84:85], v2 offset:3744
	ds_read_b64 v[116:117], v2 offset:4032
	ds_read_b64 v[114:115], v2 offset:5184
	ds_read_b64 v[112:113], v2 offset:5472
	ds_read_b64 v[90:91], v2 offset:5760
	ds_read_b32 v43, v5
	ds_read_b32 v19, v5 offset:288
	ds_read_b32 v39, v5 offset:576
	ds_read_b32 v25, v5 offset:1728
	ds_read_b32 v7, v5 offset:2016
	ds_read_b32 v21, v5 offset:2304
	ds_read_b32 v11, v5 offset:3456
	ds_read_b32 v35, v5 offset:3744
	ds_read_b32 v59, v5 offset:4032
	ds_read_b32 v57, v5 offset:5184
	ds_read_b32 v51, v5 offset:5472
	ds_read_b32 v49, v5 offset:5760
	s_waitcnt lgkmcnt(0)
	v_accvgpr_write_b32 a3, v107
	v_mov_b32_e32 v46, v43
	v_accvgpr_write_b32 a35, v75
	v_accvgpr_read_b32 v74, a40
	v_mov_b32_dpp v46, v61 row_shr:1 row_mask:0xf bank_mask:0xf
	v_mov_b32_e32 v75, v61
	v_accvgpr_read_b32 v107, a39
	v_accvgpr_write_b32 a10, v100
	v_pk_mul_f32 v[86:87], v[74:75], v[46:47]
	v_accvgpr_read_b32 v106, a38
	v_mov_b32_e32 v26, v19
	v_accvgpr_write_b32 a11, v101
	v_mov_b32_dpp v43, v60 row_shl:1 row_mask:0xf bank_mask:0xf
	v_mov_b32_e32 v32, v74
	v_pk_fma_f32 v[86:87], v[60:61], v[8:9], v[86:87] op_sel_hi:[0,1,1]
	v_pk_mov_b32 v[60:61], v[60:61], v[106:107] op_sel:[1,0]
	v_mov_b32_dpp v26, v63 row_shr:1 row_mask:0xf bank_mask:0xf
	v_accvgpr_read_b32 v74, a24
	v_mov_b32_e32 v75, v63
	v_accvgpr_read_b32 v101, a35
	v_pk_fma_f32 v[60:61], v[60:61], v[42:43], v[86:87]
	v_pk_mul_f32 v[86:87], v[74:75], v[26:27]
	v_accvgpr_read_b32 v100, a34
	v_accvgpr_write_b32 a14, v66
	v_mov_b32_dpp v19, v62 row_shl:1 row_mask:0xf bank_mask:0xf
	v_pk_fma_f32 v[86:87], v[62:63], v[126:127], v[86:87] op_sel_hi:[0,1,1]
	v_pk_mov_b32 v[62:63], v[62:63], v[100:101] op_sel:[1,0]
	v_mov_b32_e32 v44, v39
	v_accvgpr_write_b32 a42, v64
	v_accvgpr_write_b32 a15, v67
	v_mov_b32_e32 v66, v4
	v_pk_fma_f32 v[62:63], v[62:63], v[18:19], v[86:87]
	v_pk_add_f32 v[60:61], v[60:61], 0 op_sel_hi:[1,0]
	v_mov_b32_dpp v44, v69 row_shr:1 row_mask:0xf bank_mask:0xf
	v_accvgpr_read_b32 v64, a48
	v_mov_b32_e32 v65, v69
	v_accvgpr_read_b32 v4, a46
	v_pk_add_f32 v[60:61], v[60:61], v[62:63]
	v_pk_mul_f32 v[62:63], v[64:65], v[44:45]
	v_accvgpr_read_b32 v5, a47
	v_mov_b32_dpp v39, v68 row_shl:1 row_mask:0xf bank_mask:0xf
	v_pk_fma_f32 v[62:63], v[68:69], v[88:89], v[62:63] op_sel_hi:[0,1,1]
	v_pk_mov_b32 v[68:69], v[68:69], v[4:5] op_sel:[1,0]
	v_mov_b32_e32 v36, v25
	v_pk_fma_f32 v[62:63], v[68:69], v[38:39], v[62:63]
	s_mov_b64 s[0:1], 0xc00000
	v_pk_add_f32 v[60:61], v[60:61], v[62:63]
	v_mov_b32_dpp v36, v71 row_shr:1 row_mask:0xf bank_mask:0xf
	v_accvgpr_read_b32 v22, a42
	v_mov_b32_e32 v23, v71
	v_accvgpr_mov_b32 a26, a20
	v_accvgpr_write_b32 a20, v28
	v_lshl_add_u64 v[62:63], v[54:55], 0, s[0:1]
	v_mov_b32_e32 v128, v60
	v_mov_b32_e32 v129, v61
	v_pk_mul_f32 v[60:61], v[22:23], v[36:37]
	v_mov_b32_e32 v12, v7
	v_accvgpr_write_b32 a21, v29
	v_mov_b32_dpp v25, v70 row_shl:1 row_mask:0xf bank_mask:0xf
	v_pk_fma_f32 v[60:61], v[70:71], v[118:119], v[60:61] op_sel_hi:[0,1,1]
	v_mov_b32_e32 v62, v71
	v_mov_b32_e32 v63, v107
	v_mov_b32_dpp v12, v73 row_shr:1 row_mask:0xf bank_mask:0xf
	v_accvgpr_read_b32 v28, a26
	v_mov_b32_e32 v29, v73
	v_accvgpr_read_b32 v121, a3
	v_pk_fma_f32 v[60:61], v[62:63], v[24:25], v[60:61]
	v_pk_mul_f32 v[62:63], v[28:29], v[12:13]
	v_accvgpr_read_b32 v120, a2
	v_mov_b32_dpp v7, v72 row_shl:1 row_mask:0xf bank_mask:0xf
	v_pk_fma_f32 v[62:63], v[72:73], v[120:121], v[62:63] op_sel_hi:[0,1,1]
	v_mov_b32_e32 v68, v73
	v_mov_b32_e32 v69, v101
	v_mov_b32_e32 v78, v21
	v_pk_fma_f32 v[62:63], v[68:69], v[6:7], v[62:63]
	v_pk_add_f32 v[60:61], v[60:61], 0 op_sel_hi:[1,0]
	v_mov_b32_dpp v78, v83 row_shr:1 row_mask:0xf bank_mask:0xf
	v_mov_b32_e32 v53, v83
	v_accvgpr_read_b32 v125, a19
	v_pk_add_f32 v[60:61], v[60:61], v[62:63]
	v_pk_mul_f32 v[62:63], v[52:53], v[78:79]
	v_accvgpr_read_b32 v124, a18
	v_mov_b32_dpp v21, v82 row_shl:1 row_mask:0xf bank_mask:0xf
	v_pk_fma_f32 v[62:63], v[82:83], v[124:125], v[62:63] op_sel_hi:[0,1,1]
	v_mov_b32_e32 v68, v83
	v_mov_b32_e32 v69, v5
	v_pk_fma_f32 v[62:63], v[68:69], v[20:21], v[62:63]
	v_mov_b32_e32 v76, v11
	v_pk_add_f32 v[60:61], v[60:61], v[62:63]
	s_mov_b64 s[0:1], 0xc10000
	v_mov_b32_dpp v76, v81 row_shr:1 row_mask:0xf bank_mask:0xf
	v_mov_b32_e32 v41, v81
	v_accvgpr_read_b32 v123, a37
	v_accvgpr_read_b32 v4, a14
	v_lshl_add_u64 v[136:137], v[134:135], 0, s[0:1]
	s_nop 1
	s_mov_b64 vcc, s[28:29]
	s_nop 0
	v_cndmask_b32_dpp v130, v60, v128, vcc quad_perm:[1,0,3,2] row_mask:0xf bank_mask:0xf
	v_cndmask_b32_dpp v131, v61, v129, vcc quad_perm:[1,0,3,2] row_mask:0xf bank_mask:0xf
	s_mov_b64 vcc, s[30:31]
	s_nop 0
	v_cndmask_b32_dpp v132, v128, v60, vcc quad_perm:[1,0,3,2] row_mask:0xf bank_mask:0xf
	v_cndmask_b32_dpp v133, v129, v61, vcc quad_perm:[1,0,3,2] row_mask:0xf bank_mask:0xf
	global_store_dwordx4 v[136:137], v[130:133], off sc0 sc1 nt
	s_nop 1
	v_pk_mul_f32 v[60:61], v[40:41], v[76:77]
	v_accvgpr_read_b32 v122, a36
	v_accvgpr_read_b32 v5, a15
	v_mov_b32_e32 v2, v35
	v_accvgpr_mov_b32 a32, a24
	v_accvgpr_write_b32 a24, v22
	v_mov_b64_e32 v[22:23], v[118:119]
	v_mov_b32_dpp v11, v80 row_shl:1 row_mask:0xf bank_mask:0xf
	v_pk_fma_f32 v[60:61], v[80:81], v[122:123], v[60:61] op_sel_hi:[0,1,1]
	v_pk_mov_b32 v[62:63], v[80:81], v[4:5] op_sel:[1,0]
	v_mov_b32_dpp v2, v85 row_shr:1 row_mask:0xf bank_mask:0xf
	v_mov_b32_e32 v106, v0
	v_mov_b32_e32 v107, v85
	v_accvgpr_read_b32 v119, a11
	v_pk_fma_f32 v[60:61], v[62:63], v[10:11], v[60:61]
	v_pk_mul_f32 v[62:63], v[106:107], v[2:3]
	v_accvgpr_read_b32 v118, a10
	v_mov_b64_e32 v[100:101], v[14:15]
	v_mov_b32_dpp v35, v84 row_shl:1 row_mask:0xf bank_mask:0xf
	v_pk_fma_f32 v[62:63], v[84:85], v[118:119], v[62:63] op_sel_hi:[0,1,1]
	v_pk_mov_b32 v[68:69], v[84:85], v[100:101] op_sel:[1,0]
	v_mov_b32_e32 v92, v59
	v_accvgpr_write_b32 a26, v52
	v_mov_b32_e32 v74, v40
	v_pk_fma_f32 v[62:63], v[68:69], v[34:35], v[62:63]
	v_pk_add_f32 v[60:61], v[60:61], 0 op_sel_hi:[1,0]
	v_mov_b32_dpp v92, v117 row_shr:1 row_mask:0xf bank_mask:0xf
	v_mov_b32_e32 v97, v117
	v_accvgpr_read_b32 v41, a31
	v_accvgpr_read_b32 v53, a45
	v_pk_add_f32 v[60:61], v[60:61], v[62:63]
	v_pk_mul_f32 v[62:63], v[96:97], v[92:93]
	v_accvgpr_read_b32 v40, a30
	v_accvgpr_read_b32 v52, a44
	v_mov_b32_dpp v59, v116 row_shl:1 row_mask:0xf bank_mask:0xf
	v_pk_fma_f32 v[62:63], v[116:117], v[40:41], v[62:63] op_sel_hi:[0,1,1]
	v_pk_mov_b32 v[68:69], v[116:117], v[52:53] op_sel:[1,0]
	v_mov_b32_e32 v94, v57
	v_pk_fma_f32 v[62:63], v[68:69], v[58:59], v[62:63]
	s_mov_b64 s[0:1], 0xc20000
	v_pk_add_f32 v[60:61], v[60:61], v[62:63]
	v_mov_b32_dpp v94, v115 row_shr:1 row_mask:0xf bank_mask:0xf
	v_mov_b32_e32 v99, v115
	v_accvgpr_read_b32 v14, a20
	v_lshl_add_u64 v[62:63], v[54:55], 0, s[0:1]
	v_mov_b32_e32 v128, v60
	v_mov_b32_e32 v129, v61
	v_pk_mul_f32 v[60:61], v[98:99], v[94:95]
	v_accvgpr_read_b32 v15, a21
	v_mov_b32_e32 v102, v51
	v_mov_b32_dpp v57, v114 row_shl:1 row_mask:0xf bank_mask:0xf
	v_pk_fma_f32 v[60:61], v[114:115], v[14:15], v[60:61] op_sel_hi:[0,1,1]
	v_mov_b32_e32 v62, v115
	v_mov_b32_e32 v63, v5
	v_mov_b32_dpp v102, v113 row_shr:1 row_mask:0xf bank_mask:0xf
	v_mov_b32_e32 v105, v113
	v_pk_fma_f32 v[60:61], v[62:63], v[56:57], v[60:61]
	v_pk_mul_f32 v[62:63], v[104:105], v[102:103]
	v_accvgpr_write_b32 a8, v8
	v_mov_b32_dpp v51, v112 row_shl:1 row_mask:0xf bank_mask:0xf
	v_pk_fma_f32 v[62:63], v[112:113], v[16:17], v[62:63] op_sel_hi:[0,1,1]
	v_mov_b32_e32 v68, v113
	v_mov_b32_e32 v69, v101
	v_mov_b32_e32 v108, v49
	v_accvgpr_write_b32 a9, v9
	v_pk_fma_f32 v[62:63], v[68:69], v[50:51], v[62:63]
	v_pk_add_f32 v[60:61], v[60:61], 0 op_sel_hi:[1,0]
	v_mov_b32_dpp v108, v91 row_shr:1 row_mask:0xf bank_mask:0xf
	v_mov_b32_e32 v111, v91
	v_accvgpr_read_b32 v8, a22
	v_pk_add_f32 v[60:61], v[60:61], v[62:63]
	v_pk_mul_f32 v[62:63], v[110:111], v[108:109]
	v_accvgpr_read_b32 v9, a23
	v_mov_b32_dpp v49, v90 row_shl:1 row_mask:0xf bank_mask:0xf
	v_pk_fma_f32 v[62:63], v[90:91], v[8:9], v[62:63] op_sel_hi:[0,1,1]
	v_mov_b32_e32 v68, v91
	v_mov_b32_e32 v69, v53
	v_pk_fma_f32 v[62:63], v[68:69], v[48:49], v[62:63]
	s_mov_b64 s[0:1], 0xc30000
	v_pk_add_f32 v[60:61], v[60:61], v[62:63]
	v_lshl_add_u64 v[136:137], v[134:135], 0, s[0:1]
	s_nop 1
	s_mov_b64 vcc, s[28:29]
	s_nop 0
	v_cndmask_b32_dpp v130, v60, v128, vcc quad_perm:[1,0,3,2] row_mask:0xf bank_mask:0xf
	v_cndmask_b32_dpp v131, v61, v129, vcc quad_perm:[1,0,3,2] row_mask:0xf bank_mask:0xf
	s_mov_b64 vcc, s[30:31]
	s_nop 0
	v_cndmask_b32_dpp v132, v128, v60, vcc quad_perm:[1,0,3,2] row_mask:0xf bank_mask:0xf
	v_cndmask_b32_dpp v133, v129, v61, vcc quad_perm:[1,0,3,2] row_mask:0xf bank_mask:0xf
	global_store_dwordx4 v[136:137], v[130:133], off sc0 sc1 nt
	s_nop 1
	s_waitcnt vmcnt(20)
	v_accvgpr_write_b32 a16, v88
	v_accvgpr_write_b32 a10, v100
	s_waitcnt lgkmcnt(0)
	s_barrier
	v_add_u32_e32 v2, 0xe010, v31
	v_add_u32_e32 v5, 0xe000, v66
	ds_read_b64 v[60:61], v2
	ds_read_b64 v[62:63], v2 offset:288
	ds_read_b64 v[68:69], v2 offset:576
	ds_read_b64 v[70:71], v2 offset:1728
	ds_read_b64 v[72:73], v2 offset:2016
	ds_read_b64 v[82:83], v2 offset:2304
	ds_read_b64 v[80:81], v2 offset:3456
	ds_read_b64 v[84:85], v2 offset:3744
	ds_read_b64 v[116:117], v2 offset:4032
	ds_read_b64 v[114:115], v2 offset:5184
	ds_read_b64 v[112:113], v2 offset:5472
	ds_read_b64 v[90:91], v2 offset:5760
	ds_read_b32 v43, v5
	ds_read_b32 v19, v5 offset:288
	ds_read_b32 v39, v5 offset:576
	ds_read_b32 v25, v5 offset:1728
	ds_read_b32 v7, v5 offset:2016
	ds_read_b32 v21, v5 offset:2304
	ds_read_b32 v11, v5 offset:3456
	ds_read_b32 v35, v5 offset:3744
	ds_read_b32 v59, v5 offset:4032
	ds_read_b32 v57, v5 offset:5184
	ds_read_b32 v51, v5 offset:5472
	ds_read_b32 v49, v5 offset:5760
	s_waitcnt lgkmcnt(0)
	v_accvgpr_write_b32 a17, v89
	v_mov_b32_e32 v46, v43
	v_accvgpr_write_b32 a11, v101
	v_mov_b32_e32 v33, v61
	v_mov_b32_dpp v46, v61 row_shr:1 row_mask:0xf bank_mask:0xf
	v_accvgpr_read_b32 v89, a9
	v_accvgpr_read_b32 v101, a39
	v_pk_mul_f32 v[86:87], v[32:33], v[46:47]
	v_accvgpr_read_b32 v88, a8
	v_accvgpr_read_b32 v100, a38
	v_mov_b32_e32 v26, v19
	v_accvgpr_write_b32 a19, v17
	v_mov_b32_dpp v43, v60 row_shl:1 row_mask:0xf bank_mask:0xf
	v_pk_fma_f32 v[86:87], v[60:61], v[88:89], v[86:87] op_sel_hi:[0,1,1]
	v_pk_mov_b32 v[60:61], v[60:61], v[100:101] op_sel:[1,0]
	v_mov_b32_dpp v26, v63 row_shr:1 row_mask:0xf bank_mask:0xf
	v_accvgpr_read_b32 v0, a32
	v_mov_b32_e32 v1, v63
	v_accvgpr_read_b32 v4, a34
	v_accvgpr_write_b32 a18, v16
	v_pk_fma_f32 v[60:61], v[60:61], v[42:43], v[86:87]
	v_pk_mul_f32 v[86:87], v[0:1], v[26:27]
	v_mov_b64_e32 v[16:17], v[126:127]
	v_accvgpr_read_b32 v5, a35
	v_mov_b32_dpp v19, v62 row_shl:1 row_mask:0xf bank_mask:0xf
	v_pk_fma_f32 v[86:87], v[62:63], v[16:17], v[86:87] op_sel_hi:[0,1,1]
	v_pk_mov_b32 v[62:63], v[62:63], v[4:5] op_sel:[1,0]
	v_mov_b32_e32 v44, v39
	v_accvgpr_read_b32 v30, a48
	v_mov_b32_e32 v64, v28
	v_accvgpr_write_b32 a7, v66
	v_pk_fma_f32 v[62:63], v[62:63], v[18:19], v[86:87]
	v_pk_add_f32 v[60:61], v[60:61], 0 op_sel_hi:[1,0]
	v_mov_b32_dpp v44, v69 row_shr:1 row_mask:0xf bank_mask:0xf
	v_mov_b32_e32 v31, v69
	v_accvgpr_read_b32 v29, a17
	v_accvgpr_read_b32 v67, a47
	v_pk_add_f32 v[60:61], v[60:61], v[62:63]
	v_pk_mul_f32 v[62:63], v[30:31], v[44:45]
	v_accvgpr_read_b32 v28, a16
	v_accvgpr_read_b32 v66, a46
	v_mov_b32_dpp v39, v68 row_shl:1 row_mask:0xf bank_mask:0xf
	v_pk_fma_f32 v[62:63], v[68:69], v[28:29], v[62:63] op_sel_hi:[0,1,1]
	v_pk_mov_b32 v[68:69], v[68:69], v[66:67] op_sel:[1,0]
	v_mov_b32_e32 v36, v25
	v_pk_fma_f32 v[62:63], v[68:69], v[38:39], v[62:63]
	s_mov_b64 s[0:1], 0x1000000
	v_pk_add_f32 v[60:61], v[60:61], v[62:63]
	v_mov_b32_dpp v36, v71 row_shr:1 row_mask:0xf bank_mask:0xf
	v_accvgpr_read_b32 v126, a24
	v_mov_b32_e32 v127, v71
	v_lshl_add_u64 v[62:63], v[54:55], 0, s[0:1]
	v_mov_b32_e32 v128, v60
	v_mov_b32_e32 v129, v61
	v_pk_mul_f32 v[60:61], v[126:127], v[36:37]
	v_mov_b32_e32 v12, v7
	v_mov_b32_dpp v25, v70 row_shl:1 row_mask:0xf bank_mask:0xf
	v_pk_fma_f32 v[60:61], v[70:71], v[22:23], v[60:61] op_sel_hi:[0,1,1]
	v_mov_b32_e32 v62, v71
	v_mov_b32_e32 v63, v101
	v_mov_b32_dpp v12, v73 row_shr:1 row_mask:0xf bank_mask:0xf
	v_mov_b32_e32 v52, v64
	v_mov_b32_e32 v53, v73
	v_pk_fma_f32 v[60:61], v[62:63], v[24:25], v[60:61]
	v_pk_mul_f32 v[62:63], v[52:53], v[12:13]
	v_mov_b32_dpp v7, v72 row_shl:1 row_mask:0xf bank_mask:0xf
	v_pk_fma_f32 v[62:63], v[72:73], v[120:121], v[62:63] op_sel_hi:[0,1,1]
	v_mov_b32_e32 v68, v73
	v_mov_b32_e32 v69, v5
	v_mov_b32_e32 v78, v21
	v_pk_fma_f32 v[62:63], v[68:69], v[6:7], v[62:63]
	v_pk_add_f32 v[60:61], v[60:61], 0 op_sel_hi:[1,0]
	v_mov_b32_dpp v78, v83 row_shr:1 row_mask:0xf bank_mask:0xf
	v_accvgpr_read_b32 v4, a26
	v_mov_b32_e32 v5, v83
	v_pk_add_f32 v[60:61], v[60:61], v[62:63]
	v_pk_mul_f32 v[62:63], v[4:5], v[78:79]
	v_mov_b32_dpp v21, v82 row_shl:1 row_mask:0xf bank_mask:0xf
	v_pk_fma_f32 v[62:63], v[82:83], v[124:125], v[62:63] op_sel_hi:[0,1,1]
	v_mov_b32_e32 v68, v83
	v_mov_b32_e32 v69, v67
	v_accvgpr_write_b32 a8, v120
	v_pk_fma_f32 v[62:63], v[68:69], v[20:21], v[62:63]
	v_mov_b32_e32 v76, v11
	v_accvgpr_write_b32 a9, v121
	v_pk_add_f32 v[60:61], v[60:61], v[62:63]
	s_mov_b64 s[0:1], 0x1010000
	v_mov_b32_dpp v76, v81 row_shr:1 row_mask:0xf bank_mask:0xf
	v_mov_b32_e32 v120, v74
	v_mov_b32_e32 v121, v81
	v_accvgpr_read_b32 v101, a15
	v_accvgpr_mov_b32 a12, a38
	v_lshl_add_u64 v[136:137], v[134:135], 0, s[0:1]
	s_nop 1
	s_mov_b64 vcc, s[28:29]
	s_nop 0
	v_cndmask_b32_dpp v130, v60, v128, vcc quad_perm:[1,0,3,2] row_mask:0xf bank_mask:0xf
	v_cndmask_b32_dpp v131, v61, v129, vcc quad_perm:[1,0,3,2] row_mask:0xf bank_mask:0xf
	s_mov_b64 vcc, s[30:31]
	s_nop 0
	v_cndmask_b32_dpp v132, v128, v60, vcc quad_perm:[1,0,3,2] row_mask:0xf bank_mask:0xf
	v_cndmask_b32_dpp v133, v129, v61, vcc quad_perm:[1,0,3,2] row_mask:0xf bank_mask:0xf
	global_store_dwordx4 v[136:137], v[130:133], off sc0 sc1 nt
	s_nop 1
	v_pk_mul_f32 v[60:61], v[120:121], v[76:77]
	v_accvgpr_read_b32 v100, a14
	v_mov_b32_e32 v2, v35
	v_accvgpr_mov_b32 a13, a39
	v_accvgpr_write_b32 a20, v22
	v_mov_b32_dpp v11, v80 row_shl:1 row_mask:0xf bank_mask:0xf
	v_pk_fma_f32 v[60:61], v[80:81], v[122:123], v[60:61] op_sel_hi:[0,1,1]
	v_pk_mov_b32 v[62:63], v[80:81], v[100:101] op_sel:[1,0]
	v_mov_b32_dpp v2, v85 row_shr:1 row_mask:0xf bank_mask:0xf
	v_mov_b32_e32 v107, v85
	v_accvgpr_read_b32 v123, a11
	v_accvgpr_write_b32 a21, v23
	v_accvgpr_read_b32 v23, a13
	v_pk_fma_f32 v[60:61], v[62:63], v[10:11], v[60:61]
	v_pk_mul_f32 v[62:63], v[106:107], v[2:3]
	v_accvgpr_read_b32 v122, a10
	v_accvgpr_read_b32 v22, a12
	v_mov_b32_dpp v35, v84 row_shl:1 row_mask:0xf bank_mask:0xf
	v_pk_fma_f32 v[62:63], v[84:85], v[118:119], v[62:63] op_sel_hi:[0,1,1]
	v_accvgpr_write_b32 a12, v118
	v_pk_mov_b32 v[68:69], v[84:85], v[122:123] op_sel:[1,0]
	v_mov_b32_e32 v92, v59
	v_accvgpr_write_b32 a13, v119
	v_pk_fma_f32 v[62:63], v[68:69], v[34:35], v[62:63]
	v_pk_add_f32 v[60:61], v[60:61], 0 op_sel_hi:[1,0]
	v_mov_b32_dpp v92, v117 row_shr:1 row_mask:0xf bank_mask:0xf
	v_mov_b32_e32 v97, v117
	v_mov_b64_e32 v[118:119], v[40:41]
	v_accvgpr_read_b32 v40, a44
	v_pk_add_f32 v[60:61], v[60:61], v[62:63]
	v_pk_mul_f32 v[62:63], v[96:97], v[92:93]
	v_accvgpr_read_b32 v41, a45
	v_mov_b32_dpp v59, v116 row_shl:1 row_mask:0xf bank_mask:0xf
	v_pk_fma_f32 v[62:63], v[116:117], v[118:119], v[62:63] op_sel_hi:[0,1,1]
	v_pk_mov_b32 v[68:69], v[116:117], v[40:41] op_sel:[1,0]
	v_mov_b32_e32 v94, v57
	v_pk_fma_f32 v[62:63], v[68:69], v[58:59], v[62:63]
	s_mov_b64 s[0:1], 0x1020000
	v_pk_add_f32 v[60:61], v[60:61], v[62:63]
	v_mov_b32_dpp v94, v115 row_shr:1 row_mask:0xf bank_mask:0xf
	v_mov_b32_e32 v99, v115
	v_lshl_add_u64 v[62:63], v[54:55], 0, s[0:1]
	v_mov_b32_e32 v128, v60
	v_mov_b32_e32 v129, v61
	v_pk_mul_f32 v[60:61], v[98:99], v[94:95]
	v_mov_b32_e32 v102, v51
	v_accvgpr_write_b32 a30, v4
	v_mov_b32_dpp v57, v114 row_shl:1 row_mask:0xf bank_mask:0xf
	v_pk_fma_f32 v[60:61], v[114:115], v[14:15], v[60:61] op_sel_hi:[0,1,1]
	v_mov_b32_e32 v62, v115
	v_mov_b32_e32 v63, v101
	v_mov_b32_dpp v102, v113 row_shr:1 row_mask:0xf bank_mask:0xf
	v_mov_b32_e32 v105, v113
	v_accvgpr_read_b32 v4, a18
	v_pk_fma_f32 v[60:61], v[62:63], v[56:57], v[60:61]
	v_pk_mul_f32 v[62:63], v[104:105], v[102:103]
	v_accvgpr_read_b32 v5, a19
	v_mov_b32_dpp v51, v112 row_shl:1 row_mask:0xf bank_mask:0xf
	v_pk_fma_f32 v[62:63], v[112:113], v[4:5], v[62:63] op_sel_hi:[0,1,1]
	v_mov_b32_e32 v68, v113
	v_mov_b32_e32 v69, v123
	v_mov_b32_e32 v108, v49
	v_pk_fma_f32 v[62:63], v[68:69], v[50:51], v[62:63]
	v_pk_add_f32 v[60:61], v[60:61], 0 op_sel_hi:[1,0]
	v_mov_b32_dpp v108, v91 row_shr:1 row_mask:0xf bank_mask:0xf
	v_mov_b32_e32 v111, v91
	v_pk_add_f32 v[60:61], v[60:61], v[62:63]
	v_pk_mul_f32 v[62:63], v[110:111], v[108:109]
	v_mov_b32_dpp v49, v90 row_shl:1 row_mask:0xf bank_mask:0xf
	v_pk_fma_f32 v[62:63], v[90:91], v[8:9], v[62:63] op_sel_hi:[0,1,1]
	v_mov_b32_e32 v68, v91
	v_mov_b32_e32 v69, v41
	v_pk_fma_f32 v[62:63], v[68:69], v[48:49], v[62:63]
	s_mov_b64 s[0:1], 0x1030000
	v_pk_add_f32 v[60:61], v[60:61], v[62:63]
	v_lshl_add_u64 v[136:137], v[134:135], 0, s[0:1]
	s_nop 1
	s_mov_b64 vcc, s[28:29]
	s_nop 0
	v_cndmask_b32_dpp v130, v60, v128, vcc quad_perm:[1,0,3,2] row_mask:0xf bank_mask:0xf
	v_cndmask_b32_dpp v131, v61, v129, vcc quad_perm:[1,0,3,2] row_mask:0xf bank_mask:0xf
	s_mov_b64 vcc, s[30:31]
	s_nop 0
	v_cndmask_b32_dpp v132, v128, v60, vcc quad_perm:[1,0,3,2] row_mask:0xf bank_mask:0xf
	v_cndmask_b32_dpp v133, v129, v61, vcc quad_perm:[1,0,3,2] row_mask:0xf bank_mask:0xf
	global_store_dwordx4 v[136:137], v[130:133], off sc0 sc1 nt
	s_nop 1
	s_waitcnt vmcnt(16)
	s_waitcnt lgkmcnt(0)
	s_barrier
	v_accvgpr_read_b32 v2, a0
	v_accvgpr_read_b32 v8, a4
	ds_read_b64 v[60:61], v8
	ds_read_b64 v[62:63], v8 offset:288
	ds_read_b64 v[68:69], v8 offset:576
	ds_read_b64 v[70:71], v8 offset:1728
	ds_read_b64 v[72:73], v8 offset:2016
	ds_read_b64 v[82:83], v8 offset:2304
	ds_read_b64 v[80:81], v8 offset:3456
	ds_read_b64 v[84:85], v8 offset:3744
	ds_read_b64 v[116:117], v8 offset:4032
	ds_read_b64 v[114:115], v8 offset:5184
	ds_read_b64 v[112:113], v8 offset:5472
	ds_read_b64 v[90:91], v8 offset:5760
	ds_read_b32 v43, v2
	ds_read_b32 v19, v2 offset:288
	ds_read_b32 v39, v2 offset:576
	ds_read_b32 v25, v2 offset:1728
	ds_read_b32 v7, v2 offset:2016
	ds_read_b32 v21, v2 offset:2304
	ds_read_b32 v11, v2 offset:3456
	ds_read_b32 v35, v2 offset:3744
	ds_read_b32 v59, v2 offset:4032
	ds_read_b32 v57, v2 offset:5184
	ds_read_b32 v51, v2 offset:5472
	ds_read_b32 v49, v2 offset:5760
	s_waitcnt lgkmcnt(0)
	v_mov_b32_e32 v64, v32
	v_mov_b32_e32 v46, v43
	v_mov_b32_e32 v65, v61
	v_mov_b64_e32 v[100:101], v[22:23]
	v_mov_b32_dpp v46, v61 row_shr:1 row_mask:0xf bank_mask:0xf
	v_pk_mul_f32 v[86:87], v[64:65], v[46:47]
	v_mov_b32_e32 v26, v19
	v_mov_b32_dpp v43, v60 row_shl:1 row_mask:0xf bank_mask:0xf
	v_pk_fma_f32 v[86:87], v[60:61], v[88:89], v[86:87] op_sel_hi:[0,1,1]
	v_pk_mov_b32 v[60:61], v[60:61], v[100:101] op_sel:[1,0]
	v_mov_b32_dpp v26, v63 row_shr:1 row_mask:0xf bank_mask:0xf
	v_mov_b32_e32 v1, v63
	v_accvgpr_read_b32 v67, a35
	v_pk_fma_f32 v[60:61], v[60:61], v[42:43], v[86:87]
	v_pk_mul_f32 v[86:87], v[0:1], v[26:27]
	v_accvgpr_read_b32 v66, a34
	v_accvgpr_write_b32 a10, v14
	v_mov_b32_dpp v19, v62 row_shl:1 row_mask:0xf bank_mask:0xf
	v_pk_fma_f32 v[86:87], v[62:63], v[16:17], v[86:87] op_sel_hi:[0,1,1]
	v_pk_mov_b32 v[62:63], v[62:63], v[66:67] op_sel:[1,0]
	v_mov_b32_e32 v44, v39
	v_accvgpr_write_b32 a11, v15
	v_pk_fma_f32 v[62:63], v[62:63], v[18:19], v[86:87]
	v_pk_add_f32 v[60:61], v[60:61], 0 op_sel_hi:[1,0]
	v_mov_b32_dpp v44, v69 row_shr:1 row_mask:0xf bank_mask:0xf
	v_mov_b32_e32 v31, v69
	v_accvgpr_read_b32 v14, a16
	v_accvgpr_read_b32 v28, a46
	v_pk_add_f32 v[60:61], v[60:61], v[62:63]
	v_pk_mul_f32 v[62:63], v[30:31], v[44:45]
	v_accvgpr_read_b32 v15, a17
	v_accvgpr_read_b32 v29, a47
	v_mov_b32_dpp v39, v68 row_shl:1 row_mask:0xf bank_mask:0xf
	v_pk_fma_f32 v[62:63], v[68:69], v[14:15], v[62:63] op_sel_hi:[0,1,1]
	v_pk_mov_b32 v[68:69], v[68:69], v[28:29] op_sel:[1,0]
	v_mov_b32_e32 v36, v25
	v_pk_fma_f32 v[62:63], v[68:69], v[38:39], v[62:63]
	s_mov_b64 s[0:1], 0x1400000
	v_pk_add_f32 v[60:61], v[60:61], v[62:63]
	v_mov_b32_dpp v36, v71 row_shr:1 row_mask:0xf bank_mask:0xf
	v_mov_b32_e32 v127, v71
	v_accvgpr_read_b32 v8, a20
	v_lshl_add_u64 v[62:63], v[54:55], 0, s[0:1]
	v_mov_b32_e32 v128, v60
	v_mov_b32_e32 v129, v61
	v_pk_mul_f32 v[60:61], v[126:127], v[36:37]
	v_accvgpr_read_b32 v9, a21
	v_accvgpr_write_b32 a25, v23
	v_mov_b32_e32 v12, v7
	v_mov_b32_dpp v25, v70 row_shl:1 row_mask:0xf bank_mask:0xf
	v_pk_fma_f32 v[60:61], v[70:71], v[8:9], v[60:61] op_sel_hi:[0,1,1]
	v_mov_b32_e32 v62, v71
	v_mov_b32_e32 v63, v101
	v_accvgpr_write_b32 a24, v22
	v_mov_b32_dpp v12, v73 row_shr:1 row_mask:0xf bank_mask:0xf
	v_mov_b32_e32 v74, v52
	v_mov_b32_e32 v75, v73
	v_accvgpr_read_b32 v23, a9
	v_accvgpr_write_b32 a26, v124
	v_accvgpr_mov_b32 a2, a22
	v_pk_fma_f32 v[60:61], v[62:63], v[24:25], v[60:61]
	v_pk_mul_f32 v[62:63], v[74:75], v[12:13]
	v_accvgpr_read_b32 v22, a8
	v_accvgpr_write_b32 a27, v125
	v_accvgpr_mov_b32 a3, a23
	v_accvgpr_write_b32 a22, v88
	v_mov_b32_dpp v7, v72 row_shl:1 row_mask:0xf bank_mask:0xf
	v_pk_fma_f32 v[62:63], v[72:73], v[22:23], v[62:63] op_sel_hi:[0,1,1]
	v_mov_b32_e32 v68, v73
	v_mov_b32_e32 v69, v67
	v_mov_b32_e32 v78, v21
	v_accvgpr_write_b32 a23, v89
	v_pk_fma_f32 v[62:63], v[68:69], v[6:7], v[62:63]
	v_pk_add_f32 v[60:61], v[60:61], 0 op_sel_hi:[1,0]
	v_mov_b32_dpp v78, v83 row_shr:1 row_mask:0xf bank_mask:0xf
	v_accvgpr_read_b32 v52, a30
	v_mov_b32_e32 v53, v83
	v_accvgpr_read_b32 v89, a27
	v_pk_add_f32 v[60:61], v[60:61], v[62:63]
	v_pk_mul_f32 v[62:63], v[52:53], v[78:79]
	v_accvgpr_read_b32 v88, a26
	v_mov_b32_dpp v21, v82 row_shl:1 row_mask:0xf bank_mask:0xf
	v_pk_fma_f32 v[62:63], v[82:83], v[88:89], v[62:63] op_sel_hi:[0,1,1]
	v_mov_b32_e32 v68, v83
	v_mov_b32_e32 v69, v29
	v_pk_fma_f32 v[62:63], v[68:69], v[20:21], v[62:63]
	v_mov_b32_e32 v76, v11
	v_accvgpr_read_b32 v125, a37
	v_pk_add_f32 v[60:61], v[60:61], v[62:63]
	s_mov_b64 s[0:1], 0x1410000
	v_mov_b32_dpp v76, v81 row_shr:1 row_mask:0xf bank_mask:0xf
	v_mov_b32_e32 v121, v81
	v_accvgpr_read_b32 v101, a15
	v_accvgpr_read_b32 v124, a36
	v_lshl_add_u64 v[136:137], v[134:135], 0, s[0:1]
	s_nop 1
	s_mov_b64 vcc, s[28:29]
	s_nop 0
	v_cndmask_b32_dpp v130, v60, v128, vcc quad_perm:[1,0,3,2] row_mask:0xf bank_mask:0xf
	v_cndmask_b32_dpp v131, v61, v129, vcc quad_perm:[1,0,3,2] row_mask:0xf bank_mask:0xf
	s_mov_b64 vcc, s[30:31]
	s_nop 0
	v_cndmask_b32_dpp v132, v128, v60, vcc quad_perm:[1,0,3,2] row_mask:0xf bank_mask:0xf
	v_cndmask_b32_dpp v133, v129, v61, vcc quad_perm:[1,0,3,2] row_mask:0xf bank_mask:0xf
	global_store_dwordx4 v[136:137], v[130:133], off sc0 sc1 nt
	s_nop 1
	v_pk_mul_f32 v[60:61], v[120:121], v[76:77]
	v_accvgpr_read_b32 v100, a14
	v_mov_b32_e32 v2, v35
	v_mov_b32_dpp v11, v80 row_shl:1 row_mask:0xf bank_mask:0xf
	v_pk_fma_f32 v[60:61], v[80:81], v[124:125], v[60:61] op_sel_hi:[0,1,1]
	v_pk_mov_b32 v[62:63], v[80:81], v[100:101] op_sel:[1,0]
	v_mov_b32_dpp v2, v85 row_shr:1 row_mask:0xf bank_mask:0xf
	v_mov_b32_e32 v107, v85
	v_accvgpr_read_b32 v29, a13
	v_pk_fma_f32 v[60:61], v[62:63], v[10:11], v[60:61]
	v_pk_mul_f32 v[62:63], v[106:107], v[2:3]
	v_accvgpr_read_b32 v28, a12
	v_mov_b32_dpp v35, v84 row_shl:1 row_mask:0xf bank_mask:0xf
	v_pk_fma_f32 v[62:63], v[84:85], v[28:29], v[62:63] op_sel_hi:[0,1,1]
	v_pk_mov_b32 v[68:69], v[84:85], v[122:123] op_sel:[1,0]
	v_mov_b32_e32 v92, v59
	v_pk_fma_f32 v[62:63], v[68:69], v[34:35], v[62:63]
	v_pk_add_f32 v[60:61], v[60:61], 0 op_sel_hi:[1,0]
	v_mov_b32_dpp v92, v117 row_shr:1 row_mask:0xf bank_mask:0xf
	v_mov_b32_e32 v97, v117
	v_pk_add_f32 v[60:61], v[60:61], v[62:63]
	v_pk_mul_f32 v[62:63], v[96:97], v[92:93]
	v_accvgpr_write_b32 a8, v118
	v_pk_fma_f32 v[62:63], v[116:117], v[118:119], v[62:63] op_sel_hi:[0,1,1]
	v_accvgpr_write_b32 a9, v119
	v_accvgpr_read_b32 v119, a45
	v_accvgpr_read_b32 v118, a44
	v_mov_b32_dpp v59, v116 row_shl:1 row_mask:0xf bank_mask:0xf
	v_pk_mov_b32 v[68:69], v[116:117], v[118:119] op_sel:[1,0]
	v_mov_b32_e32 v94, v57
	v_pk_fma_f32 v[62:63], v[68:69], v[58:59], v[62:63]
	s_mov_b64 s[0:1], 0x1420000
	v_pk_add_f32 v[60:61], v[60:61], v[62:63]
	v_mov_b32_dpp v94, v115 row_shr:1 row_mask:0xf bank_mask:0xf
	v_mov_b32_e32 v99, v115
	v_accvgpr_read_b32 v41, a11
	v_lshl_add_u64 v[62:63], v[54:55], 0, s[0:1]
	v_mov_b32_e32 v128, v60
	v_mov_b32_e32 v129, v61
	v_pk_mul_f32 v[60:61], v[98:99], v[94:95]
	v_accvgpr_read_b32 v40, a10
	v_mov_b32_e32 v102, v51
	v_mov_b32_dpp v57, v114 row_shl:1 row_mask:0xf bank_mask:0xf
	v_pk_fma_f32 v[60:61], v[114:115], v[40:41], v[60:61] op_sel_hi:[0,1,1]
	v_mov_b32_e32 v62, v115
	v_mov_b32_e32 v63, v101
	v_mov_b32_dpp v102, v113 row_shr:1 row_mask:0xf bank_mask:0xf
	v_mov_b32_e32 v105, v113
	v_pk_fma_f32 v[60:61], v[62:63], v[56:57], v[60:61]
	v_pk_mul_f32 v[62:63], v[104:105], v[102:103]
	v_mov_b32_dpp v51, v112 row_shl:1 row_mask:0xf bank_mask:0xf
	v_pk_fma_f32 v[62:63], v[112:113], v[4:5], v[62:63] op_sel_hi:[0,1,1]
	v_mov_b32_e32 v68, v113
	v_mov_b32_e32 v69, v123
	v_mov_b32_e32 v108, v49
	v_pk_fma_f32 v[62:63], v[68:69], v[50:51], v[62:63]
	v_pk_add_f32 v[60:61], v[60:61], 0 op_sel_hi:[1,0]
	v_mov_b32_dpp v108, v91 row_shr:1 row_mask:0xf bank_mask:0xf
	v_mov_b32_e32 v111, v91
	v_accvgpr_read_b32 v5, a3
	v_pk_add_f32 v[60:61], v[60:61], v[62:63]
	v_pk_mul_f32 v[62:63], v[110:111], v[108:109]
	v_accvgpr_read_b32 v4, a2
	v_mov_b32_dpp v49, v90 row_shl:1 row_mask:0xf bank_mask:0xf
	v_pk_fma_f32 v[62:63], v[90:91], v[4:5], v[62:63] op_sel_hi:[0,1,1]
	v_mov_b32_e32 v68, v91
	v_mov_b32_e32 v69, v119
	v_pk_fma_f32 v[62:63], v[68:69], v[48:49], v[62:63]
	s_mov_b64 s[0:1], 0x1430000
	v_pk_add_f32 v[60:61], v[60:61], v[62:63]
	v_lshl_add_u64 v[136:137], v[134:135], 0, s[0:1]
	s_nop 1
	s_mov_b64 vcc, s[28:29]
	s_nop 0
	v_cndmask_b32_dpp v130, v60, v128, vcc quad_perm:[1,0,3,2] row_mask:0xf bank_mask:0xf
	v_cndmask_b32_dpp v131, v61, v129, vcc quad_perm:[1,0,3,2] row_mask:0xf bank_mask:0xf
	s_mov_b64 vcc, s[30:31]
	s_nop 0
	v_cndmask_b32_dpp v132, v128, v60, vcc quad_perm:[1,0,3,2] row_mask:0xf bank_mask:0xf
	v_cndmask_b32_dpp v133, v129, v61, vcc quad_perm:[1,0,3,2] row_mask:0xf bank_mask:0xf
	global_store_dwordx4 v[136:137], v[130:133], off sc0 sc1 nt
	s_nop 1
	s_waitcnt vmcnt(12)
	s_waitcnt lgkmcnt(0)
	s_barrier
	v_accvgpr_read_b32 v2, a1
	v_accvgpr_read_b32 v12, a5
	ds_read_b64 v[60:61], v12
	ds_read_b64 v[62:63], v12 offset:288
	ds_read_b64 v[68:69], v12 offset:576
	ds_read_b64 v[70:71], v12 offset:1728
	ds_read_b64 v[72:73], v12 offset:2016
	ds_read_b64 v[82:83], v12 offset:2304
	ds_read_b64 v[80:81], v12 offset:3456
	ds_read_b64 v[84:85], v12 offset:3744
	ds_read_b64 v[116:117], v12 offset:4032
	ds_read_b64 v[114:115], v12 offset:5184
	ds_read_b64 v[112:113], v12 offset:5472
	ds_read_b64 v[90:91], v12 offset:5760
	ds_read_b32 v43, v2
	ds_read_b32 v19, v2 offset:288
	ds_read_b32 v39, v2 offset:576
	ds_read_b32 v25, v2 offset:1728
	ds_read_b32 v7, v2 offset:2016
	ds_read_b32 v21, v2 offset:2304
	ds_read_b32 v11, v2 offset:3456
	ds_read_b32 v35, v2 offset:3744
	ds_read_b32 v59, v2 offset:4032
	ds_read_b32 v57, v2 offset:5184
	ds_read_b32 v51, v2 offset:5472
	ds_read_b32 v49, v2 offset:5760
	s_waitcnt lgkmcnt(0)
	v_accvgpr_read_b32 v101, a23
	v_mov_b32_e32 v46, v43
	v_mov_b32_e32 v65, v61
	v_accvgpr_read_b32 v31, a25
	v_mov_b32_dpp v46, v61 row_shr:1 row_mask:0xf bank_mask:0xf
	v_pk_mul_f32 v[86:87], v[64:65], v[46:47]
	v_accvgpr_read_b32 v100, a22
	v_accvgpr_read_b32 v30, a24
	v_mov_b32_e32 v26, v19
	v_mov_b32_dpp v43, v60 row_shl:1 row_mask:0xf bank_mask:0xf
	v_pk_fma_f32 v[86:87], v[60:61], v[100:101], v[86:87] op_sel_hi:[0,1,1]
	v_pk_mov_b32 v[60:61], v[60:61], v[30:31] op_sel:[1,0]
	v_mov_b32_dpp v26, v63 row_shr:1 row_mask:0xf bank_mask:0xf
	v_mov_b32_e32 v1, v63
	v_pk_fma_f32 v[60:61], v[60:61], v[42:43], v[86:87]
	v_pk_mul_f32 v[86:87], v[0:1], v[26:27]
	v_accvgpr_read_b32 v0, a34
	v_accvgpr_mov_b32 a12, a14
	v_accvgpr_read_b32 v1, a35
	v_accvgpr_mov_b32 a13, a15
	v_mov_b32_dpp v19, v62 row_shl:1 row_mask:0xf bank_mask:0xf
	v_pk_fma_f32 v[86:87], v[62:63], v[16:17], v[86:87] op_sel_hi:[0,1,1]
	v_accvgpr_write_b32 a14, v16
	v_pk_mov_b32 v[62:63], v[62:63], v[0:1] op_sel:[1,0]
	v_mov_b32_e32 v44, v39
	v_accvgpr_write_b32 a15, v17
	v_pk_fma_f32 v[62:63], v[62:63], v[18:19], v[86:87]
	v_pk_add_f32 v[60:61], v[60:61], 0 op_sel_hi:[1,0]
	v_mov_b32_dpp v44, v69 row_shr:1 row_mask:0xf bank_mask:0xf
	v_accvgpr_read_b32 v16, a48
	v_mov_b32_e32 v17, v69
	v_accvgpr_read_b32 v67, a47
	v_pk_add_f32 v[60:61], v[60:61], v[62:63]
	v_pk_mul_f32 v[62:63], v[16:17], v[44:45]
	v_accvgpr_read_b32 v66, a46
	v_mov_b32_dpp v39, v68 row_shl:1 row_mask:0xf bank_mask:0xf
	v_pk_fma_f32 v[62:63], v[68:69], v[14:15], v[62:63] op_sel_hi:[0,1,1]
	v_pk_mov_b32 v[68:69], v[68:69], v[66:67] op_sel:[1,0]
	v_mov_b32_e32 v36, v25
	v_pk_fma_f32 v[62:63], v[68:69], v[38:39], v[62:63]
	s_mov_b64 s[0:1], 0x1800000
	v_pk_add_f32 v[60:61], v[60:61], v[62:63]
	v_mov_b32_dpp v36, v71 row_shr:1 row_mask:0xf bank_mask:0xf
	v_mov_b32_e32 v127, v71
	v_lshl_add_u64 v[62:63], v[54:55], 0, s[0:1]
	v_mov_b32_e32 v128, v60
	v_mov_b32_e32 v129, v61
	v_pk_mul_f32 v[60:61], v[126:127], v[36:37]
	v_mov_b32_e32 v12, v7
	v_mov_b32_dpp v25, v70 row_shl:1 row_mask:0xf bank_mask:0xf
	v_pk_fma_f32 v[60:61], v[70:71], v[8:9], v[60:61] op_sel_hi:[0,1,1]
	v_mov_b32_e32 v62, v71
	v_mov_b32_e32 v63, v31
	v_mov_b32_dpp v12, v73 row_shr:1 row_mask:0xf bank_mask:0xf
	v_mov_b32_e32 v75, v73
	v_pk_fma_f32 v[60:61], v[62:63], v[24:25], v[60:61]
	v_pk_mul_f32 v[62:63], v[74:75], v[12:13]
	v_mov_b32_dpp v7, v72 row_shl:1 row_mask:0xf bank_mask:0xf
	v_pk_fma_f32 v[62:63], v[72:73], v[22:23], v[62:63] op_sel_hi:[0,1,1]
	v_accvgpr_write_b32 a4, v22
	v_mov_b32_e32 v68, v73
	v_mov_b32_e32 v69, v1
	v_mov_b32_e32 v78, v21
	v_accvgpr_write_b32 a5, v23
	v_pk_fma_f32 v[62:63], v[68:69], v[6:7], v[62:63]
	v_pk_add_f32 v[60:61], v[60:61], 0 op_sel_hi:[1,0]
	v_mov_b32_dpp v78, v83 row_shr:1 row_mask:0xf bank_mask:0xf
	v_mov_b32_e32 v53, v83
	v_accvgpr_read_b32 v22, a26
	v_pk_add_f32 v[60:61], v[60:61], v[62:63]
	v_pk_mul_f32 v[62:63], v[52:53], v[78:79]
	v_accvgpr_read_b32 v23, a27
	v_mov_b32_dpp v21, v82 row_shl:1 row_mask:0xf bank_mask:0xf
	v_pk_fma_f32 v[62:63], v[82:83], v[22:23], v[62:63] op_sel_hi:[0,1,1]
	v_mov_b32_e32 v68, v83
	v_mov_b32_e32 v69, v67
	v_pk_fma_f32 v[62:63], v[68:69], v[20:21], v[62:63]
	v_mov_b32_e32 v76, v11
	v_pk_add_f32 v[60:61], v[60:61], v[62:63]
	s_mov_b64 s[0:1], 0x1810000
	v_mov_b32_dpp v76, v81 row_shr:1 row_mask:0xf bank_mask:0xf
	v_mov_b32_e32 v121, v81
	v_accvgpr_read_b32 v15, a13
	v_lshl_add_u64 v[136:137], v[134:135], 0, s[0:1]
	s_nop 1
	s_mov_b64 vcc, s[28:29]
	s_nop 0
	v_cndmask_b32_dpp v130, v60, v128, vcc quad_perm:[1,0,3,2] row_mask:0xf bank_mask:0xf
	v_cndmask_b32_dpp v131, v61, v129, vcc quad_perm:[1,0,3,2] row_mask:0xf bank_mask:0xf
	s_mov_b64 vcc, s[30:31]
	s_nop 0
	v_cndmask_b32_dpp v132, v128, v60, vcc quad_perm:[1,0,3,2] row_mask:0xf bank_mask:0xf
	v_cndmask_b32_dpp v133, v129, v61, vcc quad_perm:[1,0,3,2] row_mask:0xf bank_mask:0xf
	global_store_dwordx4 v[136:137], v[130:133], off sc0 sc1 nt
	s_nop 1
	v_pk_mul_f32 v[60:61], v[120:121], v[76:77]
	v_accvgpr_read_b32 v14, a12
	v_mov_b32_e32 v2, v35
	v_mov_b32_dpp v11, v80 row_shl:1 row_mask:0xf bank_mask:0xf
	v_pk_fma_f32 v[60:61], v[80:81], v[124:125], v[60:61] op_sel_hi:[0,1,1]
	v_pk_mov_b32 v[62:63], v[80:81], v[14:15] op_sel:[1,0]
	v_mov_b32_dpp v2, v85 row_shr:1 row_mask:0xf bank_mask:0xf
	v_mov_b32_e32 v107, v85
	v_pk_fma_f32 v[60:61], v[62:63], v[10:11], v[60:61]
	v_pk_mul_f32 v[62:63], v[106:107], v[2:3]
	v_mov_b32_dpp v35, v84 row_shl:1 row_mask:0xf bank_mask:0xf
	v_pk_fma_f32 v[62:63], v[84:85], v[28:29], v[62:63] op_sel_hi:[0,1,1]
	v_pk_mov_b32 v[68:69], v[84:85], v[122:123] op_sel:[1,0]
	v_mov_b32_e32 v92, v59
	v_pk_fma_f32 v[62:63], v[68:69], v[34:35], v[62:63]
	v_pk_add_f32 v[60:61], v[60:61], 0 op_sel_hi:[1,0]
	v_mov_b32_dpp v92, v117 row_shr:1 row_mask:0xf bank_mask:0xf
	v_mov_b32_e32 v97, v117
	v_accvgpr_read_b32 v87, a9
	v_pk_add_f32 v[60:61], v[60:61], v[62:63]
	v_pk_mul_f32 v[62:63], v[96:97], v[92:93]
	v_accvgpr_read_b32 v86, a8
	v_mov_b32_dpp v59, v116 row_shl:1 row_mask:0xf bank_mask:0xf
	v_pk_fma_f32 v[62:63], v[116:117], v[86:87], v[62:63] op_sel_hi:[0,1,1]
	v_pk_mov_b32 v[68:69], v[116:117], v[118:119] op_sel:[1,0]
	v_mov_b32_e32 v94, v57
	v_pk_fma_f32 v[62:63], v[68:69], v[58:59], v[62:63]
	s_mov_b64 s[0:1], 0x1820000
	v_pk_add_f32 v[60:61], v[60:61], v[62:63]
	v_mov_b32_dpp v94, v115 row_shr:1 row_mask:0xf bank_mask:0xf
	v_mov_b32_e32 v99, v115
	v_lshl_add_u64 v[62:63], v[54:55], 0, s[0:1]
	v_mov_b32_e32 v128, v60
	v_mov_b32_e32 v129, v61
	v_pk_mul_f32 v[60:61], v[98:99], v[94:95]
	v_mov_b32_e32 v102, v51
	v_mov_b32_dpp v57, v114 row_shl:1 row_mask:0xf bank_mask:0xf
	v_pk_fma_f32 v[60:61], v[114:115], v[40:41], v[60:61] op_sel_hi:[0,1,1]
	v_mov_b32_e32 v62, v115
	v_mov_b32_e32 v63, v15
	v_mov_b32_dpp v102, v113 row_shr:1 row_mask:0xf bank_mask:0xf
	v_mov_b32_e32 v105, v113
	v_accvgpr_read_b32 v89, a19
	v_pk_fma_f32 v[60:61], v[62:63], v[56:57], v[60:61]
	v_pk_mul_f32 v[62:63], v[104:105], v[102:103]
	v_accvgpr_read_b32 v88, a18
	v_mov_b32_dpp v51, v112 row_shl:1 row_mask:0xf bank_mask:0xf
	v_pk_fma_f32 v[62:63], v[112:113], v[88:89], v[62:63] op_sel_hi:[0,1,1]
	v_mov_b32_e32 v68, v113
	v_mov_b32_e32 v69, v123
	v_mov_b32_e32 v108, v49
	v_pk_fma_f32 v[62:63], v[68:69], v[50:51], v[62:63]
	v_pk_add_f32 v[60:61], v[60:61], 0 op_sel_hi:[1,0]
	v_mov_b32_dpp v108, v91 row_shr:1 row_mask:0xf bank_mask:0xf
	v_mov_b32_e32 v111, v91
	v_pk_add_f32 v[60:61], v[60:61], v[62:63]
	v_pk_mul_f32 v[62:63], v[110:111], v[108:109]
	v_mov_b32_dpp v49, v90 row_shl:1 row_mask:0xf bank_mask:0xf
	v_pk_fma_f32 v[62:63], v[90:91], v[4:5], v[62:63] op_sel_hi:[0,1,1]
	v_mov_b32_e32 v68, v91
	v_mov_b32_e32 v69, v119
	v_pk_fma_f32 v[62:63], v[68:69], v[48:49], v[62:63]
	s_mov_b64 s[0:1], 0x1830000
	v_pk_add_f32 v[60:61], v[60:61], v[62:63]
	v_lshl_add_u64 v[136:137], v[134:135], 0, s[0:1]
	s_nop 1
	s_mov_b64 vcc, s[28:29]
	s_nop 0
	v_cndmask_b32_dpp v130, v60, v128, vcc quad_perm:[1,0,3,2] row_mask:0xf bank_mask:0xf
	v_cndmask_b32_dpp v131, v61, v129, vcc quad_perm:[1,0,3,2] row_mask:0xf bank_mask:0xf
	s_mov_b64 vcc, s[30:31]
	s_nop 0
	v_cndmask_b32_dpp v132, v128, v60, vcc quad_perm:[1,0,3,2] row_mask:0xf bank_mask:0xf
	v_cndmask_b32_dpp v133, v129, v61, vcc quad_perm:[1,0,3,2] row_mask:0xf bank_mask:0xf
	global_store_dwordx4 v[136:137], v[130:133], off sc0 sc1 nt
	s_nop 1
	v_accvgpr_write_b32 a12, v28
	s_waitcnt vmcnt(8)
	v_accvgpr_write_b32 a13, v29
	v_mov_b64_e32 v[28:29], v[4:5]
	s_waitcnt lgkmcnt(0)
	s_barrier
	v_accvgpr_read_b32 v2, a6
	v_accvgpr_read_b32 v4, a7
	ds_read_b64 v[60:61], v2
	ds_read_b64 v[62:63], v2 offset:288
	ds_read_b64 v[68:69], v2 offset:576
	ds_read_b64 v[70:71], v2 offset:1728
	ds_read_b64 v[72:73], v2 offset:2016
	ds_read_b64 v[82:83], v2 offset:2304
	ds_read_b64 v[80:81], v2 offset:3456
	ds_read_b64 v[84:85], v2 offset:3744
	ds_read_b64 v[116:117], v2 offset:4032
	ds_read_b64 v[114:115], v2 offset:5184
	ds_read_b64 v[112:113], v2 offset:5472
	ds_read_b64 v[90:91], v2 offset:5760
	ds_read_b32 v43, v4
	ds_read_b32 v19, v4 offset:288
	ds_read_b32 v39, v4 offset:576
	ds_read_b32 v25, v4 offset:1728
	ds_read_b32 v7, v4 offset:2016
	ds_read_b32 v21, v4 offset:2304
	ds_read_b32 v11, v4 offset:3456
	ds_read_b32 v35, v4 offset:3744
	ds_read_b32 v59, v4 offset:4032
	ds_read_b32 v57, v4 offset:5184
	ds_read_b32 v51, v4 offset:5472
	ds_read_b32 v49, v4 offset:5760
	s_waitcnt lgkmcnt(0)
	v_accvgpr_read_b32 v8, a24
	v_mov_b32_e32 v46, v43
	v_mov_b32_e32 v65, v61
	v_mov_b32_e32 v26, v19
	v_mov_b32_dpp v46, v61 row_shr:1 row_mask:0xf bank_mask:0xf
	v_accvgpr_read_b32 v32, a32
	v_accvgpr_read_b32 v9, a25
	v_mov_b64_e32 v[124:125], v[40:41]
	v_pk_mul_f32 v[30:31], v[64:65], v[46:47]
	v_mov_b32_dpp v26, v63 row_shr:1 row_mask:0xf bank_mask:0xf
	v_mov_b32_e32 v33, v63
	v_accvgpr_read_b32 v4, a14
	v_accvgpr_read_b32 v41, a35
	v_mov_b32_e32 v44, v39
	v_pk_fma_f32 v[30:31], v[60:61], v[100:101], v[30:31] op_sel_hi:[0,1,1]
	v_mov_b32_dpp v43, v60 row_shl:1 row_mask:0xf bank_mask:0xf
	v_pk_mov_b32 v[46:47], v[60:61], v[8:9] op_sel:[1,0]
	v_pk_mul_f32 v[26:27], v[32:33], v[26:27]
	v_accvgpr_read_b32 v5, a15
	v_accvgpr_read_b32 v40, a34
	v_mov_b32_dpp v44, v69 row_shr:1 row_mask:0xf bank_mask:0xf
	v_mov_b32_e32 v17, v69
	v_accvgpr_read_b32 v0, a16
	v_pk_fma_f32 v[30:31], v[46:47], v[42:43], v[30:31]
	v_pk_fma_f32 v[26:27], v[62:63], v[4:5], v[26:27] op_sel_hi:[0,1,1]
	v_mov_b32_dpp v19, v62 row_shl:1 row_mask:0xf bank_mask:0xf
	v_pk_mov_b32 v[32:33], v[62:63], v[40:41] op_sel:[1,0]
	v_pk_mul_f32 v[16:17], v[16:17], v[44:45]
	v_accvgpr_read_b32 v1, a17
	v_pk_fma_f32 v[18:19], v[32:33], v[18:19], v[26:27]
	v_pk_add_f32 v[26:27], v[30:31], 0 op_sel_hi:[1,0]
	v_mov_b32_dpp v39, v68 row_shl:1 row_mask:0xf bank_mask:0xf
	v_pk_fma_f32 v[16:17], v[68:69], v[0:1], v[16:17] op_sel_hi:[0,1,1]
	v_pk_mov_b32 v[30:31], v[68:69], v[66:67] op_sel:[1,0]
	v_pk_add_f32 v[18:19], v[26:27], v[18:19]
	v_pk_fma_f32 v[16:17], v[30:31], v[38:39], v[16:17]
	v_mov_b32_e32 v36, v25
	s_mov_b64 s[0:1], 0x1c00000
	v_pk_add_f32 v[16:17], v[18:19], v[16:17]
	v_mov_b32_dpp v36, v71 row_shr:1 row_mask:0xf bank_mask:0xf
	v_mov_b32_e32 v127, v71
	v_accvgpr_read_b32 v0, a20
	v_lshl_add_u64 v[26:27], v[54:55], 0, s[0:1]
	v_mov_b32_e32 v128, v16
	v_mov_b32_e32 v129, v17
	v_mov_b32_e32 v12, v7
	v_pk_mul_f32 v[16:17], v[126:127], v[36:37]
	v_accvgpr_read_b32 v1, a21
	v_mov_b32_dpp v12, v73 row_shr:1 row_mask:0xf bank_mask:0xf
	v_pk_fma_f32 v[16:17], v[70:71], v[0:1], v[16:17] op_sel_hi:[0,1,1]
	v_mov_b32_e32 v75, v73
	v_accvgpr_read_b32 v0, a4
	v_mov_b32_e32 v78, v21
	v_pk_mul_f32 v[12:13], v[74:75], v[12:13]
	v_accvgpr_read_b32 v1, a5
	v_mov_b32_dpp v25, v70 row_shl:1 row_mask:0xf bank_mask:0xf
	v_mov_b32_dpp v7, v72 row_shl:1 row_mask:0xf bank_mask:0xf
	v_mov_b32_dpp v78, v83 row_shr:1 row_mask:0xf bank_mask:0xf
	v_mov_b32_e32 v8, v71
	v_pk_fma_f32 v[12:13], v[72:73], v[0:1], v[12:13] op_sel_hi:[0,1,1]
	v_mov_b32_e32 v5, v41
	v_mov_b32_e32 v4, v73
	v_mov_b32_e32 v53, v83
	v_pk_fma_f32 v[16:17], v[8:9], v[24:25], v[16:17]
	v_pk_fma_f32 v[6:7], v[4:5], v[6:7], v[12:13]
	v_pk_mul_f32 v[12:13], v[52:53], v[78:79]
	v_mov_b32_dpp v21, v82 row_shl:1 row_mask:0xf bank_mask:0xf
	v_pk_add_f32 v[16:17], v[16:17], 0 op_sel_hi:[1,0]
	v_pk_fma_f32 v[12:13], v[82:83], v[22:23], v[12:13] op_sel_hi:[0,1,1]
	v_mov_b32_e32 v66, v83
	v_pk_add_f32 v[6:7], v[16:17], v[6:7]
	v_pk_fma_f32 v[12:13], v[66:67], v[20:21], v[12:13]
	v_mov_b32_e32 v76, v11
	v_pk_add_f32 v[6:7], v[6:7], v[12:13]
	s_mov_b64 s[0:1], 0x1c10000
	v_mov_b32_dpp v76, v81 row_shr:1 row_mask:0xf bank_mask:0xf
	v_mov_b32_e32 v121, v81
	v_accvgpr_read_b32 v0, a36
	v_lshl_add_u64 v[136:137], v[134:135], 0, s[0:1]
	s_nop 1
	s_mov_b64 vcc, s[28:29]
	s_nop 0
	v_cndmask_b32_dpp v130, v6, v128, vcc quad_perm:[1,0,3,2] row_mask:0xf bank_mask:0xf
	v_cndmask_b32_dpp v131, v7, v129, vcc quad_perm:[1,0,3,2] row_mask:0xf bank_mask:0xf
	s_mov_b64 vcc, s[30:31]
	s_nop 0
	v_cndmask_b32_dpp v132, v128, v6, vcc quad_perm:[1,0,3,2] row_mask:0xf bank_mask:0xf
	v_cndmask_b32_dpp v133, v129, v7, vcc quad_perm:[1,0,3,2] row_mask:0xf bank_mask:0xf
	global_store_dwordx4 v[136:137], v[130:133], off sc0 sc1 nt
	s_nop 1
	v_mov_b32_e32 v2, v35
	v_pk_mul_f32 v[6:7], v[120:121], v[76:77]
	v_accvgpr_read_b32 v1, a37
	v_mov_b32_dpp v2, v85 row_shr:1 row_mask:0xf bank_mask:0xf
	v_pk_fma_f32 v[6:7], v[80:81], v[0:1], v[6:7] op_sel_hi:[0,1,1]
	v_mov_b32_e32 v107, v85
	v_accvgpr_read_b32 v0, a12
	v_mov_b32_e32 v92, v59
	v_pk_mul_f32 v[2:3], v[106:107], v[2:3]
	v_accvgpr_read_b32 v1, a13
	v_mov_b32_dpp v11, v80 row_shl:1 row_mask:0xf bank_mask:0xf
	v_mov_b32_dpp v35, v84 row_shl:1 row_mask:0xf bank_mask:0xf
	v_mov_b32_dpp v92, v117 row_shr:1 row_mask:0xf bank_mask:0xf
	v_pk_mov_b32 v[8:9], v[80:81], v[14:15] op_sel:[1,0]
	v_pk_fma_f32 v[2:3], v[84:85], v[0:1], v[2:3] op_sel_hi:[0,1,1]
	v_pk_mov_b32 v[4:5], v[84:85], v[122:123] op_sel:[1,0]
	v_mov_b32_e32 v97, v117
	v_pk_fma_f32 v[6:7], v[8:9], v[10:11], v[6:7]
	v_pk_fma_f32 v[0:1], v[4:5], v[34:35], v[2:3]
	v_pk_mul_f32 v[2:3], v[96:97], v[92:93]
	v_mov_b32_dpp v59, v116 row_shl:1 row_mask:0xf bank_mask:0xf
	v_pk_add_f32 v[6:7], v[6:7], 0 op_sel_hi:[1,0]
	v_pk_fma_f32 v[2:3], v[116:117], v[86:87], v[2:3] op_sel_hi:[0,1,1]
	v_pk_mov_b32 v[4:5], v[116:117], v[118:119] op_sel:[1,0]
	v_pk_add_f32 v[0:1], v[6:7], v[0:1]
	v_pk_fma_f32 v[2:3], v[4:5], v[58:59], v[2:3]
	v_mov_b32_e32 v94, v57
	v_pk_add_f32 v[0:1], v[0:1], v[2:3]
	s_mov_b64 s[0:1], 0x1c20000
	v_mov_b32_dpp v94, v115 row_shr:1 row_mask:0xf bank_mask:0xf
	v_mov_b32_e32 v102, v51
	v_mov_b32_e32 v99, v115
	v_lshl_add_u64 v[2:3], v[54:55], 0, s[0:1]
	v_mov_b32_e32 v128, v0
	v_mov_b32_e32 v129, v1
	v_mov_b32_dpp v102, v113 row_shr:1 row_mask:0xf bank_mask:0xf
	v_pk_mul_f32 v[0:1], v[98:99], v[94:95]
	v_mov_b32_e32 v105, v113
	v_mov_b32_dpp v57, v114 row_shl:1 row_mask:0xf bank_mask:0xf
	v_pk_fma_f32 v[0:1], v[114:115], v[124:125], v[0:1] op_sel_hi:[0,1,1]
	v_mov_b32_e32 v14, v115
	v_pk_mul_f32 v[2:3], v[104:105], v[102:103]
	v_mov_b32_dpp v51, v112 row_shl:1 row_mask:0xf bank_mask:0xf
	v_mov_b32_e32 v108, v49
	v_pk_fma_f32 v[0:1], v[14:15], v[56:57], v[0:1]
	v_pk_fma_f32 v[2:3], v[112:113], v[88:89], v[2:3] op_sel_hi:[0,1,1]
	v_mov_b32_e32 v122, v113
	v_mov_b32_dpp v108, v91 row_shr:1 row_mask:0xf bank_mask:0xf
	v_pk_add_f32 v[0:1], v[0:1], 0 op_sel_hi:[1,0]
	v_pk_fma_f32 v[2:3], v[122:123], v[50:51], v[2:3]
	v_mov_b32_e32 v111, v91
	v_pk_add_f32 v[0:1], v[0:1], v[2:3]
	v_pk_mul_f32 v[2:3], v[110:111], v[108:109]
	v_mov_b32_dpp v49, v90 row_shl:1 row_mask:0xf bank_mask:0xf
	v_pk_fma_f32 v[2:3], v[90:91], v[28:29], v[2:3] op_sel_hi:[0,1,1]
	v_mov_b32_e32 v118, v91
	v_pk_fma_f32 v[2:3], v[118:119], v[48:49], v[2:3]
	s_mov_b64 s[0:1], 0x1c30000
	v_pk_add_f32 v[0:1], v[0:1], v[2:3]
	v_lshl_add_u64 v[136:137], v[134:135], 0, s[0:1]
	s_nop 1
	s_mov_b64 vcc, s[28:29]
	s_nop 0
	v_cndmask_b32_dpp v130, v0, v128, vcc quad_perm:[1,0,3,2] row_mask:0xf bank_mask:0xf
	v_cndmask_b32_dpp v131, v1, v129, vcc quad_perm:[1,0,3,2] row_mask:0xf bank_mask:0xf
	s_mov_b64 vcc, s[30:31]
	s_nop 0
	v_cndmask_b32_dpp v132, v128, v0, vcc quad_perm:[1,0,3,2] row_mask:0xf bank_mask:0xf
	v_cndmask_b32_dpp v133, v129, v1, vcc quad_perm:[1,0,3,2] row_mask:0xf bank_mask:0xf
	global_store_dwordx4 v[136:137], v[130:133], off sc0 sc1 nt
	s_nop 1
	s_endpgm
